# GDN chunk unit: diagonal-block inverses with v_pk_fma_f32 and pipelined row loads (bit-identical), wait for the unit's gathers deferred past the inverses (counted)
# baseline (speedup 1.0000x reference)
; #define LAS __attribute__((address_space(3)))
; __device__ __forceinline__ unsigned f2bf(float f) { unsigned u = __float_as_uint(f); return (u + 0x7fffu + ((u >> 16) & 1u)) >> 16; }
; __device__ __forceinline__ float rdlane_f(float v, int l) { return __builtin_bit_cast(float, __builtin_amdgcn_readlane(__builtin_bit_cast(int, v), l)); }
; __device__ __forceinline__ float gdn_s1(const GdnIn& in, LAS unsigned char* ub, LAS unsigned char* dwb, int w, int lane) {
;     ...
;     float beta = in.g2.x, cum = in.g2.y;
; #pragma unroll
;     for (int o = 1; o < 64; o <<= 1) { const float t = __shfl_up(cum, o); if (lane >= o) cum += t; }
;     const float cl = rdlane_f(cum, 63);
;     GT[lane] = beta; GT[64 + lane] = cum; GT[128 + lane] = __expf(cum);
;     asm volatile("s_waitcnt lgkmcnt(0)" ::: "memory");
;     { const f32x4 ci = *(const LAS f32x4*)(GT + 64 + 16 * I1 + 4 * kg), bi = *(const LAS f32x4*)(GT + 16 * I1 + 4 * kg);
; #pragma unroll
;       for (int jj = 0; jj < 2; ++jj) { const int J = 2 * (w & 1) + jj;
;           f32x4 ck = (f32x4){0.f, 0.f, 0.f, 0.f}, cq = (f32x4){0.f, 0.f, 0.f, 0.f};
; #pragma unroll
;           for (int s = 0; s < 2; ++s) { ck = __builtin_amdgcn_mfma_f32_16x16x32_bf16(in.ak[s], in.bk[jj][s], ck, 0, 0, 0); cq = __builtin_amdgcn_mfma_f32_16x16x32_bf16(in.aq[s], in.bk[jj][s], cq, 0, 0, 0); }
;           const int j = 16 * J + fr; const float cj = GT[64 + j];
; #pragma unroll
;           for (int e = 0; e < 4; ++e) { const int i = 16 * I1 + 4 * kg + e; const float gm = __expf(fminf(ci[e] - cj, 0.f));
;               AB[i * 72 + j] = (bf16)f2bf(j < i ? bi[e] * ck[e] * gm : 0.f); ATT[i * 72 + j] = (bf16)f2bf(j <= i ? cq[e] * gm : 0.f); } } }
.Lgf2a_done:
.LBB0_1719:
	v_mov_b32_e32 v66, v113
	v_add_u32_e32 v67, s42, v54
	s_nop 1
	v_add_f32_dpp v66, v66, v66 row_shr:1 row_mask:0xf bank_mask:0xf
	v_mfma_f32_16x16x32_bf16 v[58:61], v[6:9], v[10:13], 0
	s_nop 1
	v_add_f32_dpp v66, v66, v66 row_shr:2 row_mask:0xf bank_mask:0xf
	s_movk_i32 s2, 0x48
	s_nop 1
	v_add_f32_dpp v66, v66, v66 row_shr:4 row_mask:0xf bank_mask:0xf
	v_or_b32_e32 v69, 1, v67
	s_nop 1
	v_add_f32_dpp v66, v66, v66 row_shr:8 row_mask:0xf bank_mask:0xf
	v_or_b32_e32 v70, 2, v67
	s_nop 1
	v_add_f32_dpp v66, v66, v66 row_bcast:15 row_mask:0xa bank_mask:0xf
	s_add_i32 s28, s26, 1
	s_nop 1
	v_add_f32_dpp v66, v66, v66 row_bcast:31 row_mask:0xc bank_mask:0xf
	s_mov_b64 s[48:49], -1
	v_mul_f32_e32 v33, 0x3fb8aa3b, v66
	v_exp_f32_e32 v33, v33
	v_lshl_add_u32 v32, v110, 2, s8
	ds_write2st64_b32 v32, v112, v66 offset0:224 offset1:225
	v_readlane_b32 s36, v66, 63
	ds_write_b32 v32, v33 offset:57856
	s_waitcnt lgkmcnt(0)
	v_lshl_add_u32 v32, v54, 2, s30
	v_mfma_f32_16x16x32_bf16 v[54:57], v[2:5], v[10:13], 0
	ds_read_b128 v[50:53], v32 offset:57600
	ds_read_b128 v[46:49], v32 offset:57344
	v_or_b32_e32 v32, s43, v119
	v_lshl_add_u32 v33, v32, 2, s8
	v_add_u32_e32 v33, 0xe000, v33
	v_mfma_f32_16x16x32_bf16 v[62:65], v[18:21], v[26:29], v[54:57]
	v_cmp_lt_i32_e32 vcc, v32, v67
	s_nop 1
	ds_read2_b32 v[54:55], v33 offset0:64 offset1:80
	v_mfma_f32_16x16x32_bf16 v[56:59], v[22:25], v[26:29], v[58:61]
	s_waitcnt lgkmcnt(0)
	v_sub_f32_e32 v33, v50, v54
	v_min_f32_e32 v33, 0, v33
	v_mul_f32_e32 v33, 0x3fb8aa3b, v33
	v_exp_f32_e32 v33, v33
	v_mul_f32_e32 v60, v46, v62
	v_sub_f32_e32 v50, v50, v55
	v_min_f32_e32 v50, 0, v50
	v_mul_f32_e32 v60, v60, v33
	v_cndmask_b32_e32 v60, 0, v60, vcc
	v_bfe_u32 v61, v60, 16, 1
	v_add3_u32 v62, v60, v61, s81
	v_mad_u64_u32 v[60:61], s[2:3], v67, s2, v[32:33]
	v_cmp_gt_i32_e32 vcc, v32, v67
	v_mul_f32_e32 v33, v56, v33
	v_lshl_add_u32 v68, v60, 1, 0
	v_cndmask_b32_e64 v33, v33, 0, vcc
	v_cvt_pk_bf16_f32 v33, v33, v33
	ds_write_b16 v68, v33 offset:9216
	v_sub_f32_e32 v33, v51, v54
	v_min_f32_e32 v33, 0, v33
	v_mul_f32_e32 v33, 0x3fb8aa3b, v33
	v_exp_f32_e32 v33, v33
	v_mul_f32_e32 v56, v47, v63
	v_mul_f32_e32 v50, 0x3fb8aa3b, v50
	ds_write_b16_d16_hi v68, v62
	v_mul_f32_e32 v56, v56, v33
	v_cndmask_b32_e64 v56, v56, 0, vcc
	v_bfe_u32 v60, v56, 16, 1
	v_mul_f32_e32 v33, v57, v33
	v_cmp_le_i32_e32 vcc, v32, v69
	v_add3_u32 v56, v56, v60, s81
	ds_write_b16_d16_hi v68, v56 offset:144
	v_cndmask_b32_e32 v33, 0, v33, vcc
	v_cvt_pk_bf16_f32 v33, v33, v33
	ds_write_b16 v68, v33 offset:9360
	v_sub_f32_e32 v33, v52, v54
	v_min_f32_e32 v33, 0, v33
	v_mul_f32_e32 v33, 0x3fb8aa3b, v33
	v_exp_f32_e32 v33, v33
	v_mul_f32_e32 v56, v48, v64
	v_cmp_lt_i32_e32 vcc, v32, v70
	v_or_b32_e32 v64, 3, v67
	v_mul_f32_e32 v56, v56, v33
	v_cndmask_b32_e32 v56, 0, v56, vcc
	v_bfe_u32 v57, v56, 16, 1
	v_mul_f32_e32 v33, v58, v33
	v_cmp_le_i32_e32 vcc, v32, v70
	v_add3_u32 v56, v56, v57, s81
	ds_write_b16_d16_hi v68, v56 offset:288
	v_cndmask_b32_e32 v33, 0, v33, vcc
	v_cvt_pk_bf16_f32 v33, v33, v33
	ds_write_b16 v68, v33 offset:9504
	v_sub_f32_e32 v33, v53, v54
	v_min_f32_e32 v33, 0, v33
	v_mul_f32_e32 v33, 0x3fb8aa3b, v33
	v_exp_f32_e32 v33, v33
	v_mul_f32_e32 v54, v49, v65
	v_cmp_lt_i32_e32 vcc, v32, v64
	v_mfma_f32_16x16x32_bf16 v[60:63], v[6:9], v[14:17], 0
	v_mul_f32_e32 v54, v54, v33
	v_cndmask_b32_e32 v54, 0, v54, vcc
	v_bfe_u32 v56, v54, 16, 1
	v_add3_u32 v54, v54, v56, s81
	v_mul_f32_e32 v33, v59, v33
	v_mfma_f32_16x16x32_bf16 v[56:59], v[2:5], v[14:17], 0
	v_cmp_le_i32_e32 vcc, v32, v64
	v_exp_f32_e32 v50, v50
	ds_write_b16_d16_hi v68, v54 offset:432
	v_mfma_f32_16x16x32_bf16 v[56:59], v[18:21], v[36:39], v[56:59]
	v_cndmask_b32_e32 v33, 0, v33, vcc
	v_cvt_pk_bf16_f32 v33, v33, v33
	ds_write_b16 v68, v33 offset:9648
	v_or_b32_e32 v33, 16, v32
	s_nop 2
	s_nop 0
	v_mul_f32_e32 v46, v46, v56
	v_mfma_f32_16x16x32_bf16 v[60:63], v[22:25], v[36:39], v[60:63]
	v_cmp_lt_i32_e32 vcc, v33, v67
	v_mul_f32_e32 v46, v46, v50
	v_mul_f32_e32 v47, v47, v57
	v_cndmask_b32_e32 v46, 0, v46, vcc
	v_cvt_pk_bf16_f32 v46, v46, v46
	ds_write_b16 v68, v46 offset:32
	v_cmp_gt_i32_e32 vcc, v33, v67
	s_nop 0
	v_mul_f32_e32 v46, v60, v50
	v_mul_lo_u32 v54, v110, s75
	v_cndmask_b32_e64 v46, v46, 0, vcc
	v_cvt_pk_bf16_f32 v46, v46, v46
	ds_write_b16 v68, v46 offset:9248
	v_sub_f32_e32 v46, v51, v55
	v_min_f32_e32 v46, 0, v46
	v_mul_f32_e32 v46, 0x3fb8aa3b, v46
	v_exp_f32_e32 v46, v46
	v_lshlrev_b32_e32 v57, 16, v1
	v_lshlrev_b32_e32 v56, 16, v30
	s_mov_b32 s2, 0x7060302
	v_mul_f32_e32 v47, v47, v46
	v_cndmask_b32_e64 v47, v47, 0, vcc
	v_mul_f32_e32 v46, v61, v46
	v_cmp_le_i32_e32 vcc, v33, v69
	v_cvt_pk_bf16_f32 v47, v47, v47
	ds_write_b16 v68, v47 offset:176
	v_cndmask_b32_e32 v46, 0, v46, vcc
	v_cvt_pk_bf16_f32 v46, v46, v46
	ds_write_b16 v68, v46 offset:9392
	v_sub_f32_e32 v46, v52, v55
	v_min_f32_e32 v46, 0, v46
	v_mul_f32_e32 v46, 0x3fb8aa3b, v46
	v_exp_f32_e32 v46, v46
	v_mul_f32_e32 v47, v48, v58
	v_cmp_lt_i32_e32 vcc, v33, v70
	v_mov_b32_e32 v50, s84
	v_mul_f32_e32 v47, v47, v46
	v_cndmask_b32_e32 v47, 0, v47, vcc
	v_mul_f32_e32 v46, v62, v46
	v_cmp_le_i32_e32 vcc, v33, v70
	v_cvt_pk_bf16_f32 v47, v47, v47
	ds_write_b16 v68, v47 offset:320
	v_cndmask_b32_e32 v46, 0, v46, vcc
	v_cvt_pk_bf16_f32 v46, v46, v46
	ds_write_b16 v68, v46 offset:9536
	v_sub_f32_e32 v46, v53, v55
	v_min_f32_e32 v46, 0, v46
	v_mul_f32_e32 v46, 0x3fb8aa3b, v46
	v_exp_f32_e32 v46, v46
	v_mul_f32_e32 v47, v49, v59
	v_cmp_lt_i32_e32 vcc, v33, v64
	v_add_u32_e32 v58, s11, v54
	v_mul_f32_e32 v47, v47, v46
	v_cndmask_b32_e32 v47, 0, v47, vcc
	v_mul_f32_e32 v46, v63, v46
	v_cmp_le_i32_e32 vcc, v33, v64
	v_cvt_pk_bf16_f32 v47, v47, v47
	ds_write_b16 v68, v47 offset:464
	v_cndmask_b32_e32 v46, 0, v46, vcc
	v_cvt_pk_bf16_f32 v46, v46, v46
	ds_write_b16 v68, v46 offset:9680
	ds_read_b128 v[46:49], v50 offset:57600
	ds_read_b128 v[50:53], v50 offset:57616
	v_lshlrev_b32_e32 v55, 16, v31
	v_lshlrev_b32_e32 v54, 16, v40
	s_waitcnt lgkmcnt(1)
; #define LAS __attribute__((address_space(3)))
; __device__ __forceinline__ unsigned f2bf(float f) { unsigned u = __float_as_uint(f); return (u + 0x7fffu + ((u >> 16) & 1u)) >> 16; }
; __device__ __forceinline__ float gdn_s1(const GdnIn& in, LAS unsigned char* ub, LAS unsigned char* dwb, int w, int lane) {
;     ...
;     { const f32x4 c8a = *(const LAS f32x4*)(GT + 64 + 8 * w), c8b = *(const LAS f32x4*)(GT + 64 + 8 * w + 4);
; #pragma unroll
;       for (int tt = 0; tt < 8; ++tt) KTT[lane * 72 + 8 * w + tt] = (bf16)f2bf(__uint_as_float(in.kt8[tt] << 16) * __expf(cl - (tt < 4 ? c8a[tt & 3] : c8b[tt & 3]))); }
;     asm volatile("s_waitcnt lgkmcnt(0)" ::: "memory");
;     return cl;
; __device__ __forceinline__ void gdn_chain_units(CArgs& a, int chain, LAS unsigned char* lds, int w, int lane, unsigned long long& tacc) {
;     ...
;           __syncthreads();
;           if (PROBE_PH == 61) tacc += __builtin_amdgcn_s_memrealtime() - tq; if (PROBE_PH >= 62 && PROBE_PH <= 64) tq = __builtin_amdgcn_s_memrealtime();
;           gdn_fetch(a, chain * 36 + n + 1, w, lane, B); gdn_s23(a, chain * 36 + n, C, lds, dwb, w, lane, cl);
	v_sub_f32_e32 v46, s36, v46
	v_sub_f32_e32 v47, s36, v47
	v_sub_f32_e32 v48, s36, v48
	v_sub_f32_e32 v49, s36, v49
	v_mul_f32_e32 v46, 0x3fb8aa3b, v46
	v_mul_f32_e32 v47, 0x3fb8aa3b, v47
	v_mul_f32_e32 v48, 0x3fb8aa3b, v48
	v_mul_f32_e32 v49, 0x3fb8aa3b, v49
	v_exp_f32_e32 v46, v46
	v_exp_f32_e32 v47, v47
	v_exp_f32_e32 v48, v48
	v_exp_f32_e32 v49, v49
	s_waitcnt lgkmcnt(0)
	v_sub_f32_e32 v50, s36, v50
	v_sub_f32_e32 v51, s36, v51
	v_sub_f32_e32 v52, s36, v52
	v_sub_f32_e32 v53, s36, v53
	v_mul_f32_e32 v50, 0x3fb8aa3b, v50
	v_mul_f32_e32 v51, 0x3fb8aa3b, v51
	v_mul_f32_e32 v52, 0x3fb8aa3b, v52
	v_mul_f32_e32 v53, 0x3fb8aa3b, v53
	v_exp_f32_e32 v50, v50
	v_exp_f32_e32 v51, v51
	v_exp_f32_e32 v52, v52
	v_exp_f32_e32 v53, v53
	v_pk_mul_f32 v[46:47], v[46:47], v[56:57]
	v_pk_mul_f32 v[48:49], v[48:49], v[54:55]
	v_bfe_u32 v56, v47, 16, 1
	v_bfe_u32 v54, v49, 16, 1
	v_bfe_u32 v55, v48, 16, 1
	v_bfe_u32 v57, v46, 16, 1
	v_add3_u32 v57, v46, v57, s81
	v_add3_u32 v56, v47, v56, s81
	v_add3_u32 v55, v48, v55, s81
	v_add3_u32 v54, v49, v54, s81
	v_lshlrev_b32_e32 v47, 16, v43
	v_lshlrev_b32_e32 v46, 16, v44
	v_lshlrev_b32_e32 v49, 16, v41
	v_lshlrev_b32_e32 v48, 16, v42
	v_pk_mul_f32 v[48:49], v[50:51], v[48:49]
	v_pk_mul_f32 v[46:47], v[52:53], v[46:47]
	v_bfe_u32 v52, v49, 16, 1
	v_bfe_u32 v50, v47, 16, 1
	v_bfe_u32 v51, v46, 16, 1
	v_bfe_u32 v53, v48, 16, 1
	v_add3_u32 v48, v48, v53, s81
	v_add3_u32 v52, v49, v52, s81
	v_add3_u32 v46, v46, v51, s81
	v_add3_u32 v47, v47, v50, s81
	v_perm_b32 v49, v47, v46, s2
	v_perm_b32 v48, v52, v48, s2
	v_perm_b32 v47, v54, v55, s2
	v_perm_b32 v46, v56, v57, s2
	s_mul_hi_i32 s2, s28, 0x38e38e39
	s_lshr_b32 s3, s2, 31
	s_ashr_i32 s9, s2, 3
	s_add_i32 s9, s9, s3
	s_mul_i32 s2, s9, 36
	s_sub_i32 s2, s28, s2
	ds_write_b128 v58, v[46:49] offset:18432
	s_ashr_i32 s29, s9, 3
	s_and_b32 s27, s9, 1
	s_lshl_b32 s20, s2, 6
	s_waitcnt lgkmcnt(0)
	s_cmp_gt_i32 s2, 3
	s_cselect_b64 s[56:57], -1, 0
	s_and_b64 vcc, exec, s[56:57]
	s_waitcnt lgkmcnt(0)
	s_barrier
	s_cbranch_vccz .LBB0_1721
	s_add_i32 s2, s20, 0xffffff00
	s_lshl_b32 s3, s29, 11
	s_sub_i32 s48, 0x8ff, s20
	s_cmp_eq_u32 s27, 0
	s_cselect_b32 s2, s2, s48
	s_add_i32 s2, s3, s2
	s_addk_i32 s2, 0x1000
	s_mov_b64 s[48:49], 0

; #define LAS __attribute__((address_space(3)))
; __device__ __forceinline__ void gdn_fetch(CArgs& a, int u, int w, int lane, GdnIn& in) {
;     const int chain = u / 36, n = u % 36, b = chain >> 3, h = (chain >> 1) & 3, dir = chain & 1;
;     const int r0 = scan_row(b, dir, n * 64), step = dir ? -1 : 1, fr = lane & 15, kg = lane >> 4;
;     const float* DQ = (const float*)(a.ws + WS_MIX + MX_DQ) + h * 64; const float* DK = (const float*)(a.ws + WS_MIX + MX_DK) + h * 64; const float* DV = (const float*)(a.ws + WS_MIX + MX_DV) + h * 64;
;     const float* DG = (const float*)(a.ws + WS_MIX + MX_DG);
;     const bf16* KB = (const bf16*)(a.ws + WS_CKD + CD_KB) + (ptrdiff_t)r0 * 256 + h * 64; const bf16* QB = (const bf16*)(a.ws + WS_CKD + CD_QB) + (ptrdiff_t)r0 * 256 + h * 64;
;     const ptrdiff_t ldt = (ptrdiff_t)step * 256;
;     const bool isW = w >= 4; const int c0 = 16 * (w & 3), I1 = w >> 1;
;     in.g2 = *(const f32x2*)(DG + (size_t)(r0 + step * lane) * 16 + h * 4 + dir * 2);
; #pragma unroll
;     for (int s = 0; s < 2; ++s) { in.ak[s] = *(const bf16x8*)(KB + (ptrdiff_t)(16 * I1 + fr) * ldt + 32 * s + 8 * kg); in.aq[s] = *(const bf16x8*)(QB + (ptrdiff_t)(16 * I1 + fr) * ldt + 32 * s + 8 * kg);
; #pragma unroll
;         for (int jj = 0; jj < 2; ++jj) in.bk[jj][s] = *(const bf16x8*)(KB + (ptrdiff_t)(16 * (2 * (w & 1) + jj) + fr) * ldt + 32 * s + 8 * kg); }
; #pragma unroll
;     for (int tt = 0; tt < 8; ++tt) in.kt8[tt] = KB[(ptrdiff_t)(8 * w + tt) * ldt + lane];
; __device__ __forceinline__ void gdn_s23(CArgs& a, int u, const GdnIn2& in, LAS unsigned char* ub, LAS unsigned char* dwb, int w, int lane, float cl) {
;     ...
;     { const int blk = lane >> 4, c = lane & 15; float T[16];
; #pragma unroll
;       for (int hb = 0; hb < 4; ++hb) {
;           u32x4 arow[4][2];
; #pragma unroll
;           for (int rr = 0; rr < 4; ++rr) { const int r = 4 * hb + rr; arow[rr][0] = *(const LAS u32x4*)(AB + (16 * blk + r) * 72 + 16 * blk); if (hb >= 2) arow[rr][1] = *(const LAS u32x4*)(AB + (16 * blk + r) * 72 + 16 * blk + 8); }
;           asm volatile("s_waitcnt lgkmcnt(0)" ::: "memory");
; #pragma unroll
;           for (int rr = 0; rr < 4; ++rr) { const int r = 4 * hb + rr; float t = (r == c) ? 1.f : 0.f;
;               float t2 = 0.f;
; #pragma unroll
.LBB0_1723:
	s_bfe_u32 s76, s9, 0x20001
	s_cmp_eq_u32 s27, 0
	s_cselect_b64 s[52:53], -1, 0
	s_and_b64 s[48:49], s[52:53], exec
	s_cselect_b32 s77, 1, -1
	s_ashr_i32 s3, s2, 31
	s_lshl_b64 s[48:49], s[2:3], 9
	v_readlane_b32 s3, v251, 14
	s_add_u32 s3, s3, s48
	v_readlane_b32 s54, v249, 10
	s_addc_u32 s55, s54, s49
	s_lshl_b32 s62, s76, 7
	s_add_u32 s54, s3, s62
	s_addc_u32 s55, s55, 0
	s_add_u32 s3, s37, s48
	s_addc_u32 s49, s72, s49
	v_mul_lo_u32 v46, v110, s77
	s_add_u32 s48, s3, s62
	v_add_u32_e32 v46, s2, v46
	s_addc_u32 s49, s49, 0
	v_ashrrev_i32_e32 v47, 31, v46
	s_and_b64 s[62:63], s[52:53], exec
	s_movk_i32 s3, 0xff00
	v_lshlrev_b64 v[46:47], 6, v[46:47]
	s_cselect_b32 s62, 0x100, s3
	v_lshl_add_u64 v[46:47], s[6:7], 0, v[46:47]
	s_lshl_b32 s78, s76, 4
	v_lshl_add_u64 v[46:47], v[46:47], 0, s[78:79]
	s_lshl_b32 s78, s27, 3
	v_lshl_add_u64 v[46:47], v[46:47], 0, s[78:79]
	global_load_dwordx2 v[114:115], v[46:47], off
	v_or_b32_e32 v46, s42, v119
	v_ashrrev_i32_e32 v50, 1, v110
	v_mad_i64_i32 v[46:47], s[2:3], s62, v46, 0
	v_and_b32_e32 v50, -8, v50
	v_lshlrev_b64 v[46:47], 1, v[46:47]
	v_ashrrev_i32_e32 v51, 31, v50
	v_lshl_add_u64 v[48:49], s[54:55], 0, v[46:47]
	v_lshlrev_b64 v[50:51], 1, v[50:51]
	v_lshl_add_u64 v[46:47], s[48:49], 0, v[46:47]
	v_lshl_add_u64 v[52:53], v[48:49], 0, v[50:51]
	v_lshl_add_u64 v[54:55], v[46:47], 0, v[50:51]
	v_lshl_add_u64 v[50:51], s[54:55], 0, v[50:51]
	v_mul_hi_i32_i24_e32 v57, s62, v32
	v_mul_i32_i24_e32 v56, s62, v32
	v_lshl_add_u64 v[66:67], v[56:57], 1, v[50:51]
	v_mul_hi_i32_i24_e32 v57, s62, v33
	v_mul_i32_i24_e32 v56, s62, v33
	v_lshl_add_u64 v[32:33], v[56:57], 1, v[50:51]
	v_ashrrev_i32_e32 v111, 31, v110
	global_load_dwordx4 v[58:61], v[52:53], off
	global_load_dwordx4 v[46:49], v[54:55], off
	global_load_dwordx4 v[70:73], v[66:67], off
	global_load_dwordx4 v[62:65], v[32:33], off
	s_nop 0
	global_load_dwordx4 v[50:53], v[52:53], off offset:64
	s_nop 0
	global_load_dwordx4 v[54:57], v[54:55], off offset:64
	s_nop 0
	global_load_dwordx4 v[74:77], v[66:67], off offset:64
	s_nop 0
	global_load_dwordx4 v[66:69], v[32:33], off offset:64
	v_lshl_add_u64 v[32:33], v[110:111], 1, s[54:55]
	s_mul_hi_i32 s3, s62, s73
	s_mul_i32 s2, s62, s73
	v_lshl_add_u64 v[86:87], s[2:3], 1, v[32:33]
	s_mul_hi_i32 s3, s62, s16
	s_mul_i32 s2, s62, s16
	global_load_ushort v131, v[86:87], off
	v_lshl_add_u64 v[86:87], s[2:3], 1, v[32:33]
	s_mul_hi_i32 s3, s62, s17
	s_mul_i32 s2, s62, s17
	global_load_ushort v133, v[86:87], off
	v_lshl_add_u64 v[86:87], s[2:3], 1, v[32:33]
	s_mul_hi_i32 s3, s62, s35
	s_mul_i32 s2, s62, s35
	global_load_ushort v135, v[86:87], off
	v_lshl_add_u64 v[86:87], s[2:3], 1, v[32:33]
	s_mul_hi_i32 s3, s62, s14
	s_mul_i32 s2, s62, s14
	global_load_ushort v137, v[86:87], off
	v_lshl_add_u64 v[86:87], s[2:3], 1, v[32:33]
	s_mul_hi_i32 s3, s62, s82
	s_mul_i32 s2, s62, s82
	global_load_ushort v111, v[86:87], off
	v_lshl_add_u64 v[86:87], s[2:3], 1, v[32:33]
	s_mul_hi_i32 s3, s62, s83
	s_mul_i32 s2, s62, s83
	global_load_ushort v132, v[86:87], off
	v_lshl_add_u64 v[86:87], s[2:3], 1, v[32:33]
	s_mul_hi_i32 s3, s62, s10
	s_mul_i32 s2, s62, s10
	v_lshl_add_u64 v[32:33], s[2:3], 1, v[32:33]
	v_and_b32_e32 v85, -16, v110
	global_load_ushort v134, v[86:87], off
	global_load_ushort v136, v[32:33], off
	v_lshlrev_b32_e32 v118, 1, v119
	v_mov_b32_e32 v225, 1.0
	v_mul_u32_u24_e32 v222, 0x92, v85
	v_lshlrev_b32_e32 v224, 5, v110
	v_and_b32_e32 v224, 0xfffffe00, v224
	v_add3_u32 v223, s8, v118, v224
	v_cmp_eq_u32_e32 vcc, 0, v119
	ds_read_b128 v[86:89], v222 offset:144
	ds_read_b128 v[98:101], v222 offset:288
	ds_read_b128 v[106:109], v222 offset:432
	ds_read_b128 v[170:173], v222 offset:576
	v_cndmask_b32_e32 v202, 0, v225, vcc
	ds_write_b16_d16_hi v223, v202 offset:55296
	ds_read_b128 v[226:229], v222 offset:720
	ds_read_b128 v[234:237], v222 offset:864
	s_waitcnt lgkmcnt(5)
	v_cmp_eq_u32_e32 vcc, 1, v119
	s_nop 1
	v_cndmask_b32_e32 v218, 0, v225, vcc
	v_lshlrev_b32_e32 v220, 16, v86
	v_fma_f32 v203, -v220, v202, v218
	v_cvt_pk_bf16_f32 v224, v203, v203
	ds_write_b16 v223, v224 offset:55328
	v_cmp_eq_u32_e32 vcc, 2, v119
	v_mov_b32_e32 v219, 0
	v_lshlrev_b32_e32 v220, 16, v98
	v_and_b32_e32 v221, 0xffff0000, v98
	v_cndmask_b32_e32 v218, 0, v225, vcc
	v_pk_fma_f32 v[218:219], v[220:221], v[202:203], v[218:219] neg_lo:[1,0,0] neg_hi:[1,0,0]
	v_add_f32_e32 v204, v218, v219
	v_cvt_pk_bf16_f32 v224, v204, v204
	ds_write_b16 v223, v224 offset:55360
	ds_read_b128 v[86:89], v222 offset:1008
	ds_read_b128 v[98:101], v222 offset:1152
	s_waitcnt lgkmcnt(7)
	v_cmp_eq_u32_e32 vcc, 3, v119
	v_mov_b32_e32 v219, 0
	v_lshlrev_b32_e32 v220, 16, v106
	v_and_b32_e32 v221, 0xffff0000, v106
	v_cndmask_b32_e32 v218, 0, v225, vcc
	v_pk_fma_f32 v[218:219], v[220:221], v[202:203], v[218:219] neg_lo:[1,0,0] neg_hi:[1,0,0]
	v_lshlrev_b32_e32 v220, 16, v107
	v_fma_f32 v218, -v220, v204, v218
	v_add_f32_e32 v205, v218, v219
	v_cvt_pk_bf16_f32 v224, v205, v205
	ds_write_b16 v223, v224 offset:55392
	v_cmp_eq_u32_e32 vcc, 4, v119
	v_mov_b32_e32 v219, 0
	v_lshlrev_b32_e32 v220, 16, v170
	v_and_b32_e32 v221, 0xffff0000, v170
	v_cndmask_b32_e32 v218, 0, v225, vcc
	v_pk_fma_f32 v[218:219], v[220:221], v[202:203], v[218:219] neg_lo:[1,0,0] neg_hi:[1,0,0]
	v_lshlrev_b32_e32 v220, 16, v171
	v_and_b32_e32 v221, 0xffff0000, v171
	v_pk_fma_f32 v[218:219], v[220:221], v[204:205], v[218:219] neg_lo:[1,0,0] neg_hi:[1,0,0]
	v_add_f32_e32 v206, v218, v219
	v_cvt_pk_bf16_f32 v224, v206, v206
	ds_write_b16 v223, v224 offset:55424
	ds_read_b128 v[106:109], v222 offset:1296
	ds_read_b128 v[154:157], v222 offset:1312
	ds_read_b128 v[170:173], v222 offset:1440
	ds_read_b128 v[174:177], v222 offset:1456
	s_waitcnt lgkmcnt(10)
; #define LAS __attribute__((address_space(3)))
; __device__ __forceinline__ unsigned f2bf(float f) { unsigned u = __float_as_uint(f); return (u + 0x7fffu + ((u >> 16) & 1u)) >> 16; }
; __device__ __forceinline__ float lo_bf(unsigned w) { return __uint_as_float(w << 16); }
; __device__ __forceinline__ float hi_bf(unsigned w) { return __uint_as_float(w & 0xffff0000u); }
; __device__ __forceinline__ void gdn_s23(CArgs& a, int u, const GdnIn2& in, LAS unsigned char* ub, LAS unsigned char* dwb, int w, int lane, float cl) {
;     ...
;     { const int blk = lane >> 4, c = lane & 15; float T[16];
; #pragma unroll
;       for (int hb = 0; hb < 4; ++hb) {
;           u32x4 arow[4][2];
; #pragma unroll
;           for (int rr = 0; rr < 4; ++rr) { const int r = 4 * hb + rr; arow[rr][0] = *(const LAS u32x4*)(AB + (16 * blk + r) * 72 + 16 * blk); if (hb >= 2) arow[rr][1] = *(const LAS u32x4*)(AB + (16 * blk + r) * 72 + 16 * blk + 8); }
;           asm volatile("s_waitcnt lgkmcnt(0)" ::: "memory");
; #pragma unroll
;           for (int rr = 0; rr < 4; ++rr) { const int r = 4 * hb + rr; float t = (r == c) ? 1.f : 0.f;
;               float t2 = 0.f;
; #pragma unroll
;               for (int j = 0; j < r; ++j) { const unsigned wv = arow[rr][j >> 3][(j >> 1) & 3]; const float av = (j & 1) ? hi_bf(wv) : lo_bf(wv); if (j & 1) t2 -= av * T[j]; else t -= av * T[j]; }
;               t += t2;
;               T[r] = t; DW[(blk * 16 + r) * 16 + c] = (bf16)f2bf(t); } } }
	v_cmp_eq_u32_e32 vcc, 5, v119
	v_mov_b32_e32 v219, 0
	v_lshlrev_b32_e32 v220, 16, v226
	v_and_b32_e32 v221, 0xffff0000, v226
	v_cndmask_b32_e32 v218, 0, v225, vcc
	v_pk_fma_f32 v[218:219], v[220:221], v[202:203], v[218:219] neg_lo:[1,0,0] neg_hi:[1,0,0]
	v_lshlrev_b32_e32 v220, 16, v227
	v_and_b32_e32 v221, 0xffff0000, v227
	v_pk_fma_f32 v[218:219], v[220:221], v[204:205], v[218:219] neg_lo:[1,0,0] neg_hi:[1,0,0]
	v_lshlrev_b32_e32 v220, 16, v228
	v_fma_f32 v218, -v220, v206, v218
	v_add_f32_e32 v207, v218, v219
	v_cvt_pk_bf16_f32 v224, v207, v207
	ds_write_b16 v223, v224 offset:55456
	v_cmp_eq_u32_e32 vcc, 6, v119
	v_mov_b32_e32 v219, 0
	v_lshlrev_b32_e32 v220, 16, v234
	v_and_b32_e32 v221, 0xffff0000, v234
	v_cndmask_b32_e32 v218, 0, v225, vcc
	v_pk_fma_f32 v[218:219], v[220:221], v[202:203], v[218:219] neg_lo:[1,0,0] neg_hi:[1,0,0]
	v_lshlrev_b32_e32 v220, 16, v235
	v_and_b32_e32 v221, 0xffff0000, v235
	v_pk_fma_f32 v[218:219], v[220:221], v[204:205], v[218:219] neg_lo:[1,0,0] neg_hi:[1,0,0]
	v_lshlrev_b32_e32 v220, 16, v236
	v_and_b32_e32 v221, 0xffff0000, v236
	v_pk_fma_f32 v[218:219], v[220:221], v[206:207], v[218:219] neg_lo:[1,0,0] neg_hi:[1,0,0]
	v_add_f32_e32 v208, v218, v219
	v_cvt_pk_bf16_f32 v224, v208, v208
	ds_write_b16 v223, v224 offset:55488
	ds_read_b128 v[226:229], v222 offset:1584
	ds_read_b128 v[230:233], v222 offset:1600
	ds_read_b128 v[234:237], v222 offset:1728
	ds_read_b128 v[238:241], v222 offset:1744
	s_waitcnt lgkmcnt(12)
	v_cmp_eq_u32_e32 vcc, 7, v119
	v_mov_b32_e32 v219, 0
	v_lshlrev_b32_e32 v220, 16, v86
	v_and_b32_e32 v221, 0xffff0000, v86
	v_cndmask_b32_e32 v218, 0, v225, vcc
	v_pk_fma_f32 v[218:219], v[220:221], v[202:203], v[218:219] neg_lo:[1,0,0] neg_hi:[1,0,0]
	v_lshlrev_b32_e32 v220, 16, v87
	v_and_b32_e32 v221, 0xffff0000, v87
	v_pk_fma_f32 v[218:219], v[220:221], v[204:205], v[218:219] neg_lo:[1,0,0] neg_hi:[1,0,0]
	v_lshlrev_b32_e32 v220, 16, v88
	v_and_b32_e32 v221, 0xffff0000, v88
	v_pk_fma_f32 v[218:219], v[220:221], v[206:207], v[218:219] neg_lo:[1,0,0] neg_hi:[1,0,0]
	v_lshlrev_b32_e32 v220, 16, v89
	v_fma_f32 v218, -v220, v208, v218
	v_add_f32_e32 v209, v218, v219
	v_cvt_pk_bf16_f32 v224, v209, v209
	ds_write_b16 v223, v224 offset:55520
	v_cmp_eq_u32_e32 vcc, 8, v119
	v_mov_b32_e32 v219, 0
	v_lshlrev_b32_e32 v220, 16, v98
	v_and_b32_e32 v221, 0xffff0000, v98
	v_cndmask_b32_e32 v218, 0, v225, vcc
	v_pk_fma_f32 v[218:219], v[220:221], v[202:203], v[218:219] neg_lo:[1,0,0] neg_hi:[1,0,0]
	v_lshlrev_b32_e32 v220, 16, v99
	v_and_b32_e32 v221, 0xffff0000, v99
	v_pk_fma_f32 v[218:219], v[220:221], v[204:205], v[218:219] neg_lo:[1,0,0] neg_hi:[1,0,0]
	v_lshlrev_b32_e32 v220, 16, v100
	v_and_b32_e32 v221, 0xffff0000, v100
	v_pk_fma_f32 v[218:219], v[220:221], v[206:207], v[218:219] neg_lo:[1,0,0] neg_hi:[1,0,0]
	v_lshlrev_b32_e32 v220, 16, v101
	v_and_b32_e32 v221, 0xffff0000, v101
	v_pk_fma_f32 v[218:219], v[220:221], v[208:209], v[218:219] neg_lo:[1,0,0] neg_hi:[1,0,0]
	v_add_f32_e32 v210, v218, v219
	v_cvt_pk_bf16_f32 v224, v210, v210
	ds_write_b16 v223, v224 offset:55552
	ds_read_b128 v[86:89], v222 offset:1872
	ds_read_b128 v[94:97], v222 offset:1888
	ds_read_b128 v[98:101], v222 offset:2016
	ds_read_b128 v[102:105], v222 offset:2032
	s_waitcnt lgkmcnt(12)
	v_cmp_eq_u32_e32 vcc, 9, v119
	v_mov_b32_e32 v219, 0
	v_lshlrev_b32_e32 v220, 16, v106
	v_and_b32_e32 v221, 0xffff0000, v106
	v_cndmask_b32_e32 v218, 0, v225, vcc
	v_pk_fma_f32 v[218:219], v[220:221], v[202:203], v[218:219] neg_lo:[1,0,0] neg_hi:[1,0,0]
	v_lshlrev_b32_e32 v220, 16, v107
	v_and_b32_e32 v221, 0xffff0000, v107
	v_pk_fma_f32 v[218:219], v[220:221], v[204:205], v[218:219] neg_lo:[1,0,0] neg_hi:[1,0,0]
	v_lshlrev_b32_e32 v220, 16, v108
	v_and_b32_e32 v221, 0xffff0000, v108
	v_pk_fma_f32 v[218:219], v[220:221], v[206:207], v[218:219] neg_lo:[1,0,0] neg_hi:[1,0,0]
	v_lshlrev_b32_e32 v220, 16, v109
	v_and_b32_e32 v221, 0xffff0000, v109
	v_pk_fma_f32 v[218:219], v[220:221], v[208:209], v[218:219] neg_lo:[1,0,0] neg_hi:[1,0,0]
	v_lshlrev_b32_e32 v220, 16, v154
	v_fma_f32 v218, -v220, v210, v218
	v_add_f32_e32 v211, v218, v219
	v_cvt_pk_bf16_f32 v224, v211, v211
	ds_write_b16 v223, v224 offset:55584
	v_cmp_eq_u32_e32 vcc, 10, v119
	v_mov_b32_e32 v219, 0
	v_lshlrev_b32_e32 v220, 16, v170
	v_and_b32_e32 v221, 0xffff0000, v170
	v_cndmask_b32_e32 v218, 0, v225, vcc
	v_pk_fma_f32 v[218:219], v[220:221], v[202:203], v[218:219] neg_lo:[1,0,0] neg_hi:[1,0,0]
	v_lshlrev_b32_e32 v220, 16, v171
	v_and_b32_e32 v221, 0xffff0000, v171
	v_pk_fma_f32 v[218:219], v[220:221], v[204:205], v[218:219] neg_lo:[1,0,0] neg_hi:[1,0,0]
	v_lshlrev_b32_e32 v220, 16, v172
	v_and_b32_e32 v221, 0xffff0000, v172
	v_pk_fma_f32 v[218:219], v[220:221], v[206:207], v[218:219] neg_lo:[1,0,0] neg_hi:[1,0,0]
	v_lshlrev_b32_e32 v220, 16, v173
	v_and_b32_e32 v221, 0xffff0000, v173
	v_pk_fma_f32 v[218:219], v[220:221], v[208:209], v[218:219] neg_lo:[1,0,0] neg_hi:[1,0,0]
	v_lshlrev_b32_e32 v220, 16, v174
	v_and_b32_e32 v221, 0xffff0000, v174
	v_pk_fma_f32 v[218:219], v[220:221], v[210:211], v[218:219] neg_lo:[1,0,0] neg_hi:[1,0,0]
	v_add_f32_e32 v212, v218, v219
	v_cvt_pk_bf16_f32 v224, v212, v212
	ds_write_b16 v223, v224 offset:55616
	ds_read_b128 v[106:109], v222 offset:2160
	ds_read_b128 v[154:157], v222 offset:2176
	s_waitcnt lgkmcnt(10)
; #define LAS __attribute__((address_space(3)))
; __device__ __forceinline__ unsigned f2bf(float f) { unsigned u = __float_as_uint(f); return (u + 0x7fffu + ((u >> 16) & 1u)) >> 16; }
; __device__ __forceinline__ float lo_bf(unsigned w) { return __uint_as_float(w << 16); }
; __device__ __forceinline__ float hi_bf(unsigned w) { return __uint_as_float(w & 0xffff0000u); }
; __device__ __forceinline__ void gdn_s23(CArgs& a, int u, const GdnIn2& in, LAS unsigned char* ub, LAS unsigned char* dwb, int w, int lane, float cl) {
;     ...
;     { const int blk = lane >> 4, c = lane & 15; float T[16];
; #pragma unroll
;       for (int hb = 0; hb < 4; ++hb) {
;           u32x4 arow[4][2];
; #pragma unroll
;           for (int rr = 0; rr < 4; ++rr) { const int r = 4 * hb + rr; arow[rr][0] = *(const LAS u32x4*)(AB + (16 * blk + r) * 72 + 16 * blk); if (hb >= 2) arow[rr][1] = *(const LAS u32x4*)(AB + (16 * blk + r) * 72 + 16 * blk + 8); }
;           asm volatile("s_waitcnt lgkmcnt(0)" ::: "memory");
; #pragma unroll
;           for (int rr = 0; rr < 4; ++rr) { const int r = 4 * hb + rr; float t = (r == c) ? 1.f : 0.f;
;               float t2 = 0.f;
; #pragma unroll
;               for (int j = 0; j < r; ++j) { const unsigned wv = arow[rr][j >> 3][(j >> 1) & 3]; const float av = (j & 1) ? hi_bf(wv) : lo_bf(wv); if (j & 1) t2 -= av * T[j]; else t -= av * T[j]; }
;               t += t2;
;               T[r] = t; DW[(blk * 16 + r) * 16 + c] = (bf16)f2bf(t); } } }
;     asm volatile("s_waitcnt lgkmcnt(0)" ::: "memory");
;     f32x4 X[4];
; #pragma unroll
;     for (int I = 0; I < 4; ++I) {
;         const f32x4 br = *(const LAS f32x4*)(GT + 16 * I + 4 * kg), er = *(const LAS f32x4*)(GT + 128 + 16 * I + 4 * kg);
;         const f32x4 Rf = (f32x4){__uint_as_float(in.R[I].x << 16), __uint_as_float(in.R[I].y << 16), __uint_as_float(in.R[I].z << 16), __uint_as_float(in.R[I].w << 16)};
	v_cmp_eq_u32_e32 vcc, 11, v119
	v_mov_b32_e32 v219, 0
	v_lshlrev_b32_e32 v220, 16, v226
	v_and_b32_e32 v221, 0xffff0000, v226
	v_cndmask_b32_e32 v218, 0, v225, vcc
	v_pk_fma_f32 v[218:219], v[220:221], v[202:203], v[218:219] neg_lo:[1,0,0] neg_hi:[1,0,0]
	v_lshlrev_b32_e32 v220, 16, v227
	v_and_b32_e32 v221, 0xffff0000, v227
	v_pk_fma_f32 v[218:219], v[220:221], v[204:205], v[218:219] neg_lo:[1,0,0] neg_hi:[1,0,0]
	v_lshlrev_b32_e32 v220, 16, v228
	v_and_b32_e32 v221, 0xffff0000, v228
	v_pk_fma_f32 v[218:219], v[220:221], v[206:207], v[218:219] neg_lo:[1,0,0] neg_hi:[1,0,0]
	v_lshlrev_b32_e32 v220, 16, v229
	v_and_b32_e32 v221, 0xffff0000, v229
	v_pk_fma_f32 v[218:219], v[220:221], v[208:209], v[218:219] neg_lo:[1,0,0] neg_hi:[1,0,0]
	v_lshlrev_b32_e32 v220, 16, v230
	v_and_b32_e32 v221, 0xffff0000, v230
	v_pk_fma_f32 v[218:219], v[220:221], v[210:211], v[218:219] neg_lo:[1,0,0] neg_hi:[1,0,0]
	v_lshlrev_b32_e32 v220, 16, v231
	v_fma_f32 v218, -v220, v212, v218
	v_add_f32_e32 v213, v218, v219
	v_cvt_pk_bf16_f32 v224, v213, v213
	ds_write_b16 v223, v224 offset:55648
	v_cmp_eq_u32_e32 vcc, 12, v119
	v_mov_b32_e32 v219, 0
	v_lshlrev_b32_e32 v220, 16, v234
	v_and_b32_e32 v221, 0xffff0000, v234
	v_cndmask_b32_e32 v218, 0, v225, vcc
	v_pk_fma_f32 v[218:219], v[220:221], v[202:203], v[218:219] neg_lo:[1,0,0] neg_hi:[1,0,0]
	v_lshlrev_b32_e32 v220, 16, v235
	v_and_b32_e32 v221, 0xffff0000, v235
	v_pk_fma_f32 v[218:219], v[220:221], v[204:205], v[218:219] neg_lo:[1,0,0] neg_hi:[1,0,0]
	v_lshlrev_b32_e32 v220, 16, v236
	v_and_b32_e32 v221, 0xffff0000, v236
	v_pk_fma_f32 v[218:219], v[220:221], v[206:207], v[218:219] neg_lo:[1,0,0] neg_hi:[1,0,0]
	v_lshlrev_b32_e32 v220, 16, v237
	v_and_b32_e32 v221, 0xffff0000, v237
	v_pk_fma_f32 v[218:219], v[220:221], v[208:209], v[218:219] neg_lo:[1,0,0] neg_hi:[1,0,0]
	v_lshlrev_b32_e32 v220, 16, v238
	v_and_b32_e32 v221, 0xffff0000, v238
	v_pk_fma_f32 v[218:219], v[220:221], v[210:211], v[218:219] neg_lo:[1,0,0] neg_hi:[1,0,0]
	v_lshlrev_b32_e32 v220, 16, v239
	v_and_b32_e32 v221, 0xffff0000, v239
	v_pk_fma_f32 v[218:219], v[220:221], v[212:213], v[218:219] neg_lo:[1,0,0] neg_hi:[1,0,0]
	v_add_f32_e32 v214, v218, v219
	v_cvt_pk_bf16_f32 v224, v214, v214
	ds_write_b16 v223, v224 offset:55680
	s_waitcnt lgkmcnt(6)
	v_cmp_eq_u32_e32 vcc, 13, v119
	v_mov_b32_e32 v219, 0
	v_lshlrev_b32_e32 v220, 16, v86
	v_and_b32_e32 v221, 0xffff0000, v86
	v_cndmask_b32_e32 v218, 0, v225, vcc
	v_pk_fma_f32 v[218:219], v[220:221], v[202:203], v[218:219] neg_lo:[1,0,0] neg_hi:[1,0,0]
	v_lshlrev_b32_e32 v220, 16, v87
	v_and_b32_e32 v221, 0xffff0000, v87
	v_pk_fma_f32 v[218:219], v[220:221], v[204:205], v[218:219] neg_lo:[1,0,0] neg_hi:[1,0,0]
	v_lshlrev_b32_e32 v220, 16, v88
	v_and_b32_e32 v221, 0xffff0000, v88
	v_pk_fma_f32 v[218:219], v[220:221], v[206:207], v[218:219] neg_lo:[1,0,0] neg_hi:[1,0,0]
	v_lshlrev_b32_e32 v220, 16, v89
	v_and_b32_e32 v221, 0xffff0000, v89
	v_pk_fma_f32 v[218:219], v[220:221], v[208:209], v[218:219] neg_lo:[1,0,0] neg_hi:[1,0,0]
	v_lshlrev_b32_e32 v220, 16, v94
	v_and_b32_e32 v221, 0xffff0000, v94
	v_pk_fma_f32 v[218:219], v[220:221], v[210:211], v[218:219] neg_lo:[1,0,0] neg_hi:[1,0,0]
	v_lshlrev_b32_e32 v220, 16, v95
	v_and_b32_e32 v221, 0xffff0000, v95
	v_pk_fma_f32 v[218:219], v[220:221], v[212:213], v[218:219] neg_lo:[1,0,0] neg_hi:[1,0,0]
	v_lshlrev_b32_e32 v220, 16, v96
	v_fma_f32 v218, -v220, v214, v218
	v_add_f32_e32 v215, v218, v219
	v_cvt_pk_bf16_f32 v224, v215, v215
	ds_write_b16 v223, v224 offset:55712
	v_cmp_eq_u32_e32 vcc, 14, v119
	v_mov_b32_e32 v219, 0
	v_lshlrev_b32_e32 v220, 16, v98
	v_and_b32_e32 v221, 0xffff0000, v98
	v_cndmask_b32_e32 v218, 0, v225, vcc
	v_pk_fma_f32 v[218:219], v[220:221], v[202:203], v[218:219] neg_lo:[1,0,0] neg_hi:[1,0,0]
	v_lshlrev_b32_e32 v220, 16, v99
	v_and_b32_e32 v221, 0xffff0000, v99
	v_pk_fma_f32 v[218:219], v[220:221], v[204:205], v[218:219] neg_lo:[1,0,0] neg_hi:[1,0,0]
	v_lshlrev_b32_e32 v220, 16, v100
	v_and_b32_e32 v221, 0xffff0000, v100
	v_pk_fma_f32 v[218:219], v[220:221], v[206:207], v[218:219] neg_lo:[1,0,0] neg_hi:[1,0,0]
	v_lshlrev_b32_e32 v220, 16, v101
	v_and_b32_e32 v221, 0xffff0000, v101
	v_pk_fma_f32 v[218:219], v[220:221], v[208:209], v[218:219] neg_lo:[1,0,0] neg_hi:[1,0,0]
	v_lshlrev_b32_e32 v220, 16, v102
	v_and_b32_e32 v221, 0xffff0000, v102
	v_pk_fma_f32 v[218:219], v[220:221], v[210:211], v[218:219] neg_lo:[1,0,0] neg_hi:[1,0,0]
	v_lshlrev_b32_e32 v220, 16, v103
	v_and_b32_e32 v221, 0xffff0000, v103
	v_pk_fma_f32 v[218:219], v[220:221], v[212:213], v[218:219] neg_lo:[1,0,0] neg_hi:[1,0,0]
	v_lshlrev_b32_e32 v220, 16, v104
	v_and_b32_e32 v221, 0xffff0000, v104
	v_pk_fma_f32 v[218:219], v[220:221], v[214:215], v[218:219] neg_lo:[1,0,0] neg_hi:[1,0,0]
	v_add_f32_e32 v216, v218, v219
	v_cvt_pk_bf16_f32 v224, v216, v216
	ds_write_b16 v223, v224 offset:55744
	s_waitcnt lgkmcnt(4)
	v_cmp_eq_u32_e32 vcc, 15, v119
	v_mov_b32_e32 v219, 0
	v_lshlrev_b32_e32 v220, 16, v106
	v_and_b32_e32 v221, 0xffff0000, v106
	v_cndmask_b32_e32 v218, 0, v225, vcc
	v_pk_fma_f32 v[218:219], v[220:221], v[202:203], v[218:219] neg_lo:[1,0,0] neg_hi:[1,0,0]
	v_lshlrev_b32_e32 v220, 16, v107
	v_and_b32_e32 v221, 0xffff0000, v107
	v_pk_fma_f32 v[218:219], v[220:221], v[204:205], v[218:219] neg_lo:[1,0,0] neg_hi:[1,0,0]
	v_lshlrev_b32_e32 v220, 16, v108
	v_and_b32_e32 v221, 0xffff0000, v108
	v_pk_fma_f32 v[218:219], v[220:221], v[206:207], v[218:219] neg_lo:[1,0,0] neg_hi:[1,0,0]
	v_lshlrev_b32_e32 v220, 16, v109
	v_and_b32_e32 v221, 0xffff0000, v109
	v_pk_fma_f32 v[218:219], v[220:221], v[208:209], v[218:219] neg_lo:[1,0,0] neg_hi:[1,0,0]
	v_lshlrev_b32_e32 v220, 16, v154
	v_and_b32_e32 v221, 0xffff0000, v154
	v_pk_fma_f32 v[218:219], v[220:221], v[210:211], v[218:219] neg_lo:[1,0,0] neg_hi:[1,0,0]
	v_lshlrev_b32_e32 v220, 16, v155
	v_and_b32_e32 v221, 0xffff0000, v155
	v_pk_fma_f32 v[218:219], v[220:221], v[212:213], v[218:219] neg_lo:[1,0,0] neg_hi:[1,0,0]
	v_lshlrev_b32_e32 v220, 16, v156
	v_and_b32_e32 v221, 0xffff0000, v156
	v_pk_fma_f32 v[218:219], v[220:221], v[214:215], v[218:219] neg_lo:[1,0,0] neg_hi:[1,0,0]
	v_lshlrev_b32_e32 v220, 16, v157
	v_fma_f32 v218, -v220, v216, v218
	v_add_f32_e32 v217, v218, v219
	v_cvt_pk_bf16_f32 v224, v217, v217
	ds_write_b16 v223, v224 offset:55776
	s_waitcnt vmcnt(17)
; #define LAS __attribute__((address_space(3)))
; __device__ __forceinline__ u32x2 cvt4(f32x4 v) { return (u32x2){pk2(v[0], v[1]), pk2(v[2], v[3])}; }
; __device__ __forceinline__ void gdn_s23(CArgs& a, int u, const GdnIn2& in, LAS unsigned char* ub, LAS unsigned char* dwb, int w, int lane, float cl) {
;     ...
;     asm volatile("s_waitcnt lgkmcnt(0)" ::: "memory");
;     f32x4 X[4];
; #pragma unroll
;     for (int I = 0; I < 4; ++I) {
;         const f32x4 br = *(const LAS f32x4*)(GT + 16 * I + 4 * kg), er = *(const LAS f32x4*)(GT + 128 + 16 * I + 4 * kg);
;         const f32x4 Rf = (f32x4){__uint_as_float(in.R[I].x << 16), __uint_as_float(in.R[I].y << 16), __uint_as_float(in.R[I].z << 16), __uint_as_float(in.R[I].w << 16)};
;         f32x4 acc = isW ? br * er * Rf : br * Rf;
; #pragma unroll
;         for (int P = 0; 2 * P < I; ++P) {
;             const u32x2 alo = *(const LAS u32x2*)(AB + (16 * I + fr) * 72 + 32 * P + 4 * kg);
;             const u32x2 ahi = (2 * P + 1 < I) ? *(const LAS u32x2*)(AB + (16 * I + fr) * 72 + 32 * P + 16 + 4 * kg) : (u32x2){0u, 0u};
;             const u32x2 xlo = cvt4(-X[2 * P]); const u32x2 xhi = (2 * P + 1 < I) ? cvt4(-X[2 * P + 1]) : (u32x2){0u, 0u};
;             acc = __builtin_amdgcn_mfma_f32_16x16x32_bf16(frag2(alo, ahi), frag2(xlo, xhi), acc, 0, 0, 0); }
;         const u32x2 dlo = *(const LAS u32x2*)(DW + (I * 16 + fr) * 16 + 4 * kg);
;         X[I] = __builtin_amdgcn_mfma_f32_16x16x32_bf16(frag2(dlo, (u32x2){0u, 0u}), frag2(cvt4(acc), (u32x2){0u, 0u}), (f32x4){0.f, 0.f, 0.f, 0.f}, 0, 0, 0);
;     }
	v_lshlrev_b32_e32 v151, 16, v151
	v_lshlrev_b32_e32 v150, 16, v150
	v_lshlrev_b32_e32 v153, 16, v153
	v_lshlrev_b32_e32 v152, 16, v152
	v_lshlrev_b32_e32 v147, 16, v147
	v_lshlrev_b32_e32 v146, 16, v146
	v_lshlrev_b32_e32 v149, 16, v149
	v_lshlrev_b32_e32 v148, 16, v148
	v_lshlrev_b32_e32 v144, 16, v144
	v_lshlrev_b32_e32 v142, 16, v142
	v_lshlrev_b32_e32 v145, 16, v145
	v_lshlrev_b32_e32 v143, 16, v143
	v_lshlrev_b32_e32 v140, 16, v140
	v_lshlrev_b32_e32 v138, 16, v138
	v_lshlrev_b32_e32 v141, 16, v141
	v_lshlrev_b32_e32 v139, 16, v139
	s_waitcnt lgkmcnt(0)
	v_add_u32_e32 v157, s8, v85
	ds_read_b128 v[94:97], v157 offset:57344
	ds_read_b128 v[86:89], v157 offset:57856
	v_ashrrev_i32_e32 v123, 4, v110
	v_lshlrev_b32_e32 v104, 3, v123
	v_lshlrev_b32_e32 v33, 16, v82
	v_lshlrev_b32_e32 v82, 16, v83
	v_lshlrev_b32_e32 v83, 16, v84
	s_waitcnt lgkmcnt(0)
	v_pk_mul_f32 v[84:85], v[96:97], v[88:89]
	v_pk_mul_f32 v[98:99], v[94:95], v[86:87]
	v_sub_u32_e32 v158, v157, v104
	v_lshlrev_b32_e32 v32, 16, v34
	v_cndmask_b32_e64 v85, v97, v85, s[38:39]
	v_cndmask_b32_e64 v84, v96, v84, s[38:39]
	v_cndmask_b32_e64 v95, v95, v99, s[38:39]
	v_cndmask_b32_e64 v94, v94, v98, s[38:39]
	v_pk_mul_f32 v[84:85], v[84:85], v[82:83]
	v_pk_mul_f32 v[82:83], v[94:95], v[32:33]
	v_lshl_add_u32 v32, v119, 5, v158
	ds_read_b64 v[32:33], v32 offset:55296
	v_cvt_pk_bf16_f32 v82, v82, v82
	v_bfe_u32 v94, v83, 16, 1
	v_mov_b32_e32 v34, v35
	v_lshrrev_b32_e32 v82, 16, v82
	v_add3_u32 v83, v83, v94, s81
	v_and_or_b32 v82, v83, s80, v82
	v_cvt_pk_bf16_f32 v83, v84, v85
	v_mov_b32_e32 v84, v35
	v_mov_b32_e32 v85, v35
	v_or_b32_e32 v156, 16, v119
	v_add_u32_e32 v154, 0, v104
	s_waitcnt lgkmcnt(0)
	v_mfma_f32_16x16x32_bf16 v[94:97], v[32:35], v[82:85], 0
	ds_read_b128 v[98:101], v157 offset:57408
	ds_read_b128 v[82:85], v157 offset:57920
	v_lshlrev_b32_e32 v32, 16, v78
	s_waitcnt vmcnt(27)
	v_lshlrev_b32_e32 v33, 16, v79
	s_waitcnt vmcnt(26)
	v_lshlrev_b32_e32 v78, 16, v80
	s_waitcnt vmcnt(25)
	v_lshlrev_b32_e32 v79, 16, v81
	s_waitcnt lgkmcnt(0)
	v_pk_mul_f32 v[80:81], v[100:101], v[84:85]
	v_pk_mul_f32 v[102:103], v[98:99], v[82:83]
	v_cndmask_b32_e64 v81, v101, v81, s[38:39]
	v_cndmask_b32_e64 v80, v100, v80, s[38:39]
	v_cndmask_b32_e64 v99, v99, v103, s[38:39]
	v_cndmask_b32_e64 v98, v98, v102, s[38:39]
	v_xor_b32_e32 v100, 0x80000000, v95
	v_pk_mul_f32 v[80:81], v[80:81], v[78:79]
	v_pk_mul_f32 v[78:79], v[98:99], v[32:33]
	v_xor_b32_e32 v99, 0x80000000, v94
	v_bfe_u32 v101, v100, 16, 1
	v_add3_u32 v100, v100, v101, s81
	v_bfe_u32 v101, v99, 16, 1
	v_add3_u32 v99, v99, v101, s81
	v_mad_u32_u24 v159, v156, s75, v154
	v_xor_b32_e32 v98, 0x80000000, v97
	v_lshrrev_b32_e32 v99, 16, v99
	ds_read_b64 v[32:33], v159
	v_xor_b32_e32 v34, 0x80000000, v96
	v_and_or_b32 v106, v100, s80, v99
	v_cvt_pk_bf16_f32 v98, v98, v98
	v_bfe_u32 v99, v34, 16, 1
	v_add3_u32 v34, v34, v99, s81
	v_lshrrev_b32_e32 v34, 16, v34
	v_and_or_b32 v107, v98, s80, v34
	v_mov_b32_e32 v34, v35
	v_mov_b32_e32 v108, v35
	v_mov_b32_e32 v109, v35
	v_or_b32_e32 v155, 32, v119
	s_ashr_i32 s27, s26, 31
	s_waitcnt lgkmcnt(0)
	v_mfma_f32_16x16x32_bf16 v[78:81], v[32:35], v[106:109], v[78:81]
	v_lshl_add_u32 v32, v156, 5, v158
	ds_read_b64 v[32:33], v32 offset:55296
	s_lshl_b64 s[76:77], s[26:27], 13
	s_add_u32 s62, s85, s76
	s_addc_u32 s63, s64, s77
	s_nop 2
	v_cvt_pk_bf16_f32 v78, v78, v78
	v_bfe_u32 v98, v79, 16, 1
	v_lshrrev_b32_e32 v78, 16, v78
	v_add3_u32 v79, v79, v98, s81
	v_and_or_b32 v78, v79, s80, v78
	v_cvt_pk_bf16_f32 v79, v80, v81
	v_mov_b32_e32 v80, v35
	v_mov_b32_e32 v81, v35
	s_add_u32 s48, s71, s76
	s_addc_u32 s49, s18, s77
	s_waitcnt lgkmcnt(0)
	v_mfma_f32_16x16x32_bf16 v[98:101], v[32:35], v[78:81], 0
	ds_read_b128 v[102:105], v157 offset:57472
	ds_read_b128 v[78:81], v157 offset:57984
	s_waitcnt vmcnt(24)
	v_lshlrev_b32_e32 v32, 16, v90
	s_waitcnt vmcnt(23)
	v_lshlrev_b32_e32 v33, 16, v91
	s_waitcnt vmcnt(22)
	v_lshlrev_b32_e32 v90, 16, v92
	s_waitcnt vmcnt(21)
	v_lshlrev_b32_e32 v91, 16, v93
	s_waitcnt lgkmcnt(0)
	v_pk_mul_f32 v[92:93], v[104:105], v[80:81]
	v_pk_mul_f32 v[108:109], v[102:103], v[78:79]
	v_cndmask_b32_e64 v93, v105, v93, s[38:39]
	v_cndmask_b32_e64 v92, v104, v92, s[38:39]
	v_cndmask_b32_e64 v103, v103, v109, s[38:39]
	v_cndmask_b32_e64 v102, v102, v108, s[38:39]
	v_pk_mul_f32 v[92:93], v[92:93], v[90:91]
	v_pk_mul_f32 v[90:91], v[102:103], v[32:33]
	v_add_u32_e32 v32, 0x800, v159
	v_xor_b32_e32 v108, 0x80000000, v99
	ds_read2_b64 v[102:105], v32 offset0:32 offset1:36
	v_xor_b32_e32 v34, 0x80000000, v98
	v_xor_b32_e32 v33, 0x80000000, v101
	v_xor_b32_e32 v32, 0x80000000, v100
	v_cvt_pk_bf16_f32 v108, v34, v108
	v_cvt_pk_bf16_f32 v109, v32, v33
	v_lshl_add_u32 v32, v155, 5, v158
	ds_read_b64 v[32:33], v32 offset:55296
	s_waitcnt lgkmcnt(1)
; #define LAS __attribute__((address_space(3)))
; __device__ __forceinline__ u32x2 cvt4(f32x4 v) { return (u32x2){pk2(v[0], v[1]), pk2(v[2], v[3])}; }
; __device__ __forceinline__ void gdn_s23(CArgs& a, int u, const GdnIn2& in, LAS unsigned char* ub, LAS unsigned char* dwb, int w, int lane, float cl) {
;     ...
; #pragma unroll
;         for (int P = 0; 2 * P < I; ++P) {
;             const u32x2 alo = *(const LAS u32x2*)(AB + (16 * I + fr) * 72 + 32 * P + 4 * kg);
;             const u32x2 ahi = (2 * P + 1 < I) ? *(const LAS u32x2*)(AB + (16 * I + fr) * 72 + 32 * P + 16 + 4 * kg) : (u32x2){0u, 0u};
;             const u32x2 xlo = cvt4(-X[2 * P]); const u32x2 xhi = (2 * P + 1 < I) ? cvt4(-X[2 * P + 1]) : (u32x2){0u, 0u};
;             acc = __builtin_amdgcn_mfma_f32_16x16x32_bf16(frag2(alo, ahi), frag2(xlo, xhi), acc, 0, 0, 0); }
;         const u32x2 dlo = *(const LAS u32x2*)(DW + (I * 16 + fr) * 16 + 4 * kg);
;         X[I] = __builtin_amdgcn_mfma_f32_16x16x32_bf16(frag2(dlo, (u32x2){0u, 0u}), frag2(cvt4(acc), (u32x2){0u, 0u}), (f32x4){0.f, 0.f, 0.f, 0.f}, 0, 0, 0);
;     }
;     const bf16x8 Xb01 = frag2(cvt4(X[0]), cvt4(X[1])), Xb23 = frag2(cvt4(X[2]), cvt4(X[3]));
;     const float ecl = __expf(cl);
;     bf16* ftp = FTo + (c0 + fr) * 64 + 4 * kg; bf16* btp = BTo + (c0 + fr) * 64 + 4 * kg; bf16* ep = Eo + (4 * kg) * 64 + c0 + fr; bf16* mp = Mo + (4 * kg) * 64 + c0 + fr;
; #pragma unroll
;     for (int t4 = 0; t4 < 4; ++t4) {
;         const LAS bf16* ar = ATT + (16 * t4 + fr) * 72 + 4 * kg; const LAS bf16* kr = KTT + (16 * t4 + fr) * 72 + 4 * kg;
;         f32x4 pa = (f32x4){0.f, 0.f, 0.f, 0.f}, pk = (f32x4){0.f, 0.f, 0.f, 0.f};
;         pa = __builtin_amdgcn_mfma_f32_16x16x32_bf16(frag2(*(const LAS u32x2*)ar, *(const LAS u32x2*)(ar + 16)), Xb01, pa, 0, 0, 0);
;         pa = __builtin_amdgcn_mfma_f32_16x16x32_bf16(frag2(*(const LAS u32x2*)(ar + 32), *(const LAS u32x2*)(ar + 48)), Xb23, pa, 0, 0, 0);
;         pk = __builtin_amdgcn_mfma_f32_16x16x32_bf16(frag2(*(const LAS u32x2*)kr, *(const LAS u32x2*)(kr + 16)), Xb01, pk, 0, 0, 0);
;         pk = __builtin_amdgcn_mfma_f32_16x16x32_bf16(frag2(*(const LAS u32x2*)(kr + 32), *(const LAS u32x2*)(kr + 48)), Xb23, pk, 0, 0, 0);
;         if (!isW) {
;             *(u32x2*)(ftp + 16 * t4) = cvt4(pa);
;             *(u32x2*)(btp + 16 * t4) = cvt4(pk);
	v_mfma_f32_16x16x32_bf16 v[90:93], v[102:105], v[106:109], v[90:93]
	v_mov_b32_e32 v34, v35
	s_add_u32 s2, s19, s76
	v_lshlrev_b32_e32 v116, 2, v123
	s_addc_u32 s3, s66, s77
	s_add_u32 s54, s21, s76
	s_nop 2
	v_cvt_pk_bf16_f32 v90, v90, v90
	v_bfe_u32 v102, v91, 16, 1
	v_lshrrev_b32_e32 v90, 16, v90
	v_add3_u32 v91, v91, v102, s81
	v_and_or_b32 v90, v91, s80, v90
	v_cvt_pk_bf16_f32 v91, v92, v93
	v_mov_b32_e32 v92, v35
	v_mov_b32_e32 v93, v35
	s_addc_u32 s55, s70, s77
	s_mov_b64 s[76:77], -1
	s_waitcnt lgkmcnt(0)
	v_mfma_f32_16x16x32_bf16 v[102:105], v[32:35], v[90:93], 0
	ds_read_b128 v[170:173], v157 offset:57536
	ds_read_b128 v[90:93], v157 offset:58048
	s_waitcnt vmcnt(20)
	v_lshlrev_b32_e32 v32, 16, v117
	s_waitcnt vmcnt(19)
	v_lshlrev_b32_e32 v33, 16, v120
	s_waitcnt vmcnt(18)
	v_lshlrev_b32_e32 v120, 16, v121
	s_waitcnt vmcnt(17)
	v_lshlrev_b32_e32 v121, 16, v122
	s_waitcnt lgkmcnt(0)
	v_pk_mul_f32 v[174:175], v[170:171], v[90:91]
	v_pk_mul_f32 v[162:163], v[172:173], v[92:93]
	v_cndmask_b32_e64 v171, v171, v175, s[38:39]
	v_cndmask_b32_e64 v170, v170, v174, s[38:39]
	v_pk_mul_f32 v[170:171], v[170:171], v[32:33]
	v_add_u32_e32 v32, 0x1000, v159
	ds_read2_b64 v[174:177], v32 offset0:64 offset1:68
	v_cndmask_b32_e64 v163, v173, v163, s[38:39]
	v_cndmask_b32_e64 v162, v172, v162, s[38:39]
	v_pk_mul_f32 v[172:173], v[162:163], v[120:121]
	v_xor_b32_e32 v121, 0x80000000, v103
	v_xor_b32_e32 v120, 0x80000000, v102
	v_cvt_pk_bf16_f32 v121, v121, v121
	v_cvt_pk_bf16_f32 v120, v120, v120
	v_xor_b32_e32 v117, 0x80000000, v105
	v_lshrrev_b32_e32 v120, 16, v120
	s_waitcnt lgkmcnt(0)
	v_mfma_f32_16x16x32_bf16 v[106:109], v[174:177], v[106:109], v[170:173]
	ds_read_b64 v[32:33], v159 offset:4672
	v_xor_b32_e32 v34, 0x80000000, v104
	v_or_b32_e32 v157, 48, v119
	v_and_or_b32 v170, v121, s80, v120
	v_cvt_pk_bf16_f32 v171, v34, v117
	v_mov_b32_e32 v34, v35
	v_mov_b32_e32 v172, v35
	v_mov_b32_e32 v173, v35
	s_andn2_b64 vcc, exec, s[60:61]
	s_waitcnt lgkmcnt(0)
	v_mfma_f32_16x16x32_bf16 v[106:109], v[32:35], v[170:173], v[106:109]
	v_lshl_add_u32 v32, v157, 5, v158
	ds_read_b64 v[32:33], v32 offset:55296
	s_nop 5
	v_cvt_pk_bf16_f32 v106, v106, v107
	v_cvt_pk_bf16_f32 v107, v108, v109
	v_mov_b32_e32 v108, v35
	v_mov_b32_e32 v109, v35
	v_ashrrev_i32_e32 v117, 31, v116
	s_waitcnt lgkmcnt(0)
	v_mfma_f32_16x16x32_bf16 v[106:109], v[32:35], v[106:109], 0
	v_cvt_pk_bf16_f32 v94, v94, v95
	v_cvt_pk_bf16_f32 v95, v96, v97
	v_cvt_pk_bf16_f32 v96, v98, v99
	v_cvt_pk_bf16_f32 v97, v100, v101
	v_cvt_pk_bf16_f32 v98, v102, v103
	v_cvt_pk_bf16_f32 v99, v104, v105
	s_nop 1
	v_cvt_pk_bf16_f32 v100, v106, v107
	v_lshlrev_b32_e32 v34, 7, v45
	v_cvt_pk_bf16_f32 v101, v108, v109
	v_lshl_add_u64 v[32:33], s[48:49], 0, v[34:35]
	v_lshlrev_b64 v[102:103], 1, v[116:117]
	v_lshl_add_u64 v[120:121], v[32:33], 0, v[102:103]
	v_lshl_add_u64 v[32:33], s[54:55], 0, v[34:35]
	v_mul_u32_u24_e32 v34, 0x48, v119
	v_lshl_add_u32 v34, v34, 1, v154
	v_add_u32_e32 v106, 0x2000, v34
	v_lshl_add_u64 v[32:33], v[32:33], 0, v[102:103]
	ds_read2_b64 v[102:105], v106 offset0:128 offset1:132
	ds_read2_b64 v[106:109], v106 offset0:136 offset1:140
	s_waitcnt lgkmcnt(1)
	v_mfma_f32_16x16x32_bf16 v[102:105], v[102:105], v[94:97], 0
	v_add_u32_e32 v34, 0x4800, v34
	ds_read2_b64 v[170:173], v34 offset0:8 offset1:12
	s_waitcnt lgkmcnt(1)
	v_mfma_f32_16x16x32_bf16 v[102:105], v[106:109], v[98:101], v[102:105]
	ds_read2_b64 v[106:109], v34 offset1:4
	v_cndmask_b32_e64 v34, 0, 1, s[60:61]
	v_cmp_ne_u32_e64 s[48:49], 1, v34
	s_waitcnt lgkmcnt(0)
	v_mfma_f32_16x16x32_bf16 v[106:109], v[106:109], v[94:97], 0
	v_mfma_f32_16x16x32_bf16 v[106:109], v[170:173], v[98:101], v[106:109]
	s_cbranch_vccnz .LBB0_1725
	s_nop 0
	v_cvt_pk_bf16_f32 v158, v102, v103
	v_cvt_pk_bf16_f32 v159, v104, v105
	global_store_dwordx2 v[120:121], v[158:159], off
	s_nop 2
	v_cvt_pk_bf16_f32 v158, v106, v107
	v_cvt_pk_bf16_f32 v34, v108, v108
	v_bfe_u32 v117, v109, 16, 1
	v_lshrrev_b32_e32 v34, 16, v34
	v_add3_u32 v117, v109, v117, s81
	v_and_or_b32 v159, v117, s80, v34
	s_mov_b64 s[76:77], 0
	global_store_dwordx2 v[32:33], v[158:159], off

; #define LAS __attribute__((address_space(3)))
; __device__ __forceinline__ unsigned f2bf(float f) { unsigned u = __float_as_uint(f); return (u + 0x7fffu + ((u >> 16) & 1u)) >> 16; }
; __device__ __forceinline__ float rdlane_f(float v, int l) { return __builtin_bit_cast(float, __builtin_amdgcn_readlane(__builtin_bit_cast(int, v), l)); }
; __device__ __forceinline__ float gdn_s1(const GdnIn& in, LAS unsigned char* ub, LAS unsigned char* dwb, int w, int lane) {
;     ...
;     float beta = in.g2.x, cum = in.g2.y;
; #pragma unroll
;     for (int o = 1; o < 64; o <<= 1) { const float t = __shfl_up(cum, o); if (lane >= o) cum += t; }
;     const float cl = rdlane_f(cum, 63);
;     GT[lane] = beta; GT[64 + lane] = cum; GT[128 + lane] = __expf(cum);
;     asm volatile("s_waitcnt lgkmcnt(0)" ::: "memory");
;     { const f32x4 ci = *(const LAS f32x4*)(GT + 64 + 16 * I1 + 4 * kg), bi = *(const LAS f32x4*)(GT + 16 * I1 + 4 * kg);
; #pragma unroll
;       for (int jj = 0; jj < 2; ++jj) { const int J = 2 * (w & 1) + jj;
;           f32x4 ck = (f32x4){0.f, 0.f, 0.f, 0.f}, cq = (f32x4){0.f, 0.f, 0.f, 0.f};
; #pragma unroll
;           for (int s = 0; s < 2; ++s) { ck = __builtin_amdgcn_mfma_f32_16x16x32_bf16(in.ak[s], in.bk[jj][s], ck, 0, 0, 0); cq = __builtin_amdgcn_mfma_f32_16x16x32_bf16(in.aq[s], in.bk[jj][s], cq, 0, 0, 0); }
;           const int j = 16 * J + fr; const float cj = GT[64 + j];
; #pragma unroll
;           for (int e = 0; e < 4; ++e) { const int i = 16 * I1 + 4 * kg + e; const float gm = __expf(fminf(ci[e] - cj, 0.f));
;               AB[i * 72 + j] = (bf16)f2bf(j < i ? bi[e] * ck[e] * gm : 0.f); ATT[i * 72 + j] = (bf16)f2bf(j <= i ? cq[e] * gm : 0.f); } } }
.Lgf2b_done:
.LBB0_1775:
	s_waitcnt vmcnt(32)
	v_mov_b32_e32 v33, v115
	s_waitcnt vmcnt(29)
	v_mfma_f32_16x16x32_bf16 v[86:89], v[58:61], v[70:73], 0
	s_movk_i32 s2, 0x48
	v_add_f32_dpp v33, v33, v33 row_shr:1 row_mask:0xf bank_mask:0xf
	s_cmp_gt_u32 s0, 33
	v_mfma_f32_16x16x32_bf16 v[70:73], v[46:49], v[70:73], 0
	v_add_f32_dpp v33, v33, v33 row_shr:2 row_mask:0xf bank_mask:0xf
	s_cselect_b64 s[50:51], -1, 0
	s_nop 1
	v_add_f32_dpp v33, v33, v33 row_shr:4 row_mask:0xf bank_mask:0xf
	s_mov_b64 s[62:63], 0x40000
	s_waitcnt vmcnt(25)
	v_add_f32_dpp v33, v33, v33 row_shr:8 row_mask:0xf bank_mask:0xf
	v_mfma_f32_16x16x32_bf16 v[86:89], v[50:53], v[74:77], v[86:89]
	s_nop 1
	v_add_f32_dpp v33, v33, v33 row_bcast:15 row_mask:0xa bank_mask:0xf
	v_mfma_f32_16x16x32_bf16 v[70:73], v[54:57], v[74:77], v[70:73]
	v_mfma_f32_16x16x32_bf16 v[46:49], v[46:49], v[62:65], 0
	v_add_f32_dpp v33, v33, v33 row_bcast:31 row_mask:0xc bank_mask:0xf
	v_mfma_f32_16x16x32_bf16 v[58:61], v[58:61], v[62:65], 0
	v_mul_f32_e32 v78, 0x3fb8aa3b, v33
	v_exp_f32_e32 v78, v78
	v_lshl_add_u32 v32, v110, 2, s8
	ds_write2st64_b32 v32, v114, v33 offset0:224 offset1:225
	v_add_u32_e32 v114, s42, v34
	ds_write_b32 v32, v78 offset:57856
	s_waitcnt lgkmcnt(0)
	v_lshl_add_u32 v32, v34, 2, s30
	ds_read_b128 v[82:85], v32 offset:57600
	ds_read_b128 v[78:81], v32 offset:57344
	v_or_b32_e32 v32, s43, v106
	v_lshl_add_u32 v34, v32, 2, s8
	v_add_u32_e32 v34, 0xe000, v34
	ds_read2_b32 v[74:75], v34 offset0:64 offset1:80
	s_waitcnt lgkmcnt(1)
	v_mul_f32_e32 v76, v78, v86
	v_cmp_lt_i32_e32 vcc, v32, v114
	s_waitcnt vmcnt(24)
	v_mfma_f32_16x16x32_bf16 v[46:49], v[54:57], v[66:69], v[46:49]
	v_readlane_b32 s9, v33, 63
	s_waitcnt lgkmcnt(0)
	v_sub_f32_e32 v34, v82, v74
	v_min_f32_e32 v34, 0, v34
	v_mul_f32_e32 v34, 0x3fb8aa3b, v34
	v_exp_f32_e32 v34, v34
	v_sub_f32_e32 v54, v82, v75
	v_min_f32_e32 v54, 0, v54
	v_mfma_f32_16x16x32_bf16 v[50:53], v[50:53], v[66:69], v[58:61]
	v_mul_f32_e32 v76, v76, v34
	v_cndmask_b32_e32 v76, 0, v76, vcc
	v_cmp_gt_i32_e32 vcc, v32, v114
	v_mul_f32_e32 v34, v70, v34
	s_nop 0
	v_cndmask_b32_e64 v34, v34, 0, vcc
	v_cvt_pk_bf16_f32 v86, v76, v76
	v_mad_u64_u32 v[76:77], s[2:3], v114, s2, v[32:33]
	v_lshl_add_u32 v76, v76, 1, 0
	v_cvt_pk_bf16_f32 v34, v34, v34
	ds_write_b16 v76, v34 offset:36864
	v_sub_f32_e32 v34, v83, v74
	v_min_f32_e32 v34, 0, v34
	v_mul_f32_e32 v34, 0x3fb8aa3b, v34
	v_exp_f32_e32 v34, v34
	v_mul_f32_e32 v77, v79, v87
	v_or_b32_e32 v70, 1, v114
	ds_write_b16 v76, v86 offset:27648
	v_mul_f32_e32 v77, v77, v34
	v_cndmask_b32_e64 v77, v77, 0, vcc
	v_mul_f32_e32 v34, v71, v34
	v_cmp_le_i32_e32 vcc, v32, v70
	v_cvt_pk_bf16_f32 v77, v77, v77
	s_nop 0
	v_cndmask_b32_e32 v34, 0, v34, vcc
	v_cvt_pk_bf16_f32 v34, v34, v34
	ds_write_b16 v76, v34 offset:37008
	v_sub_f32_e32 v34, v84, v74
	v_min_f32_e32 v34, 0, v34
	v_mul_f32_e32 v34, 0x3fb8aa3b, v34
	v_exp_f32_e32 v34, v34
	ds_write_b16 v76, v77 offset:27792
	v_or_b32_e32 v71, 2, v114
	v_mul_f32_e32 v77, v80, v88
	v_cmp_lt_i32_e32 vcc, v32, v71
	v_mul_f32_e32 v77, v77, v34
	v_mul_f32_e32 v34, v72, v34
	v_cndmask_b32_e32 v77, 0, v77, vcc
	v_cmp_le_i32_e32 vcc, v32, v71
	v_mul_f32_e32 v54, 0x3fb8aa3b, v54
	v_exp_f32_e32 v54, v54
	v_cndmask_b32_e32 v34, 0, v34, vcc
	v_cvt_pk_bf16_f32 v34, v34, v34
	ds_write_b16 v76, v34 offset:37152
	v_sub_f32_e32 v34, v85, v74
	v_min_f32_e32 v34, 0, v34
	v_mul_f32_e32 v34, 0x3fb8aa3b, v34
	v_exp_f32_e32 v34, v34
	v_or_b32_e32 v72, 3, v114
	v_mul_f32_e32 v74, v81, v89
	v_cmp_lt_i32_e32 vcc, v32, v72
	v_mul_f32_e32 v74, v74, v34
	v_mul_f32_e32 v34, v73, v34
	v_cndmask_b32_e32 v74, 0, v74, vcc
	v_cmp_le_i32_e32 vcc, v32, v72
	v_mul_f32_e32 v50, v78, v50
	v_mul_f32_e32 v50, v50, v54
	v_cndmask_b32_e32 v34, 0, v34, vcc
	v_cvt_pk_bf16_f32 v34, v34, v34
	ds_write_b16_d16_hi v76, v34 offset:37296
	v_or_b32_e32 v34, 16, v32
	v_cmp_lt_i32_e32 vcc, v34, v114
	v_mul_f32_e32 v46, v46, v54
	v_bfe_u32 v86, v77, 16, 1
	v_cndmask_b32_e32 v50, 0, v50, vcc
	v_cmp_gt_i32_e32 vcc, v34, v114
	v_cvt_pk_bf16_f32 v50, v50, v50
	ds_write_b16 v76, v50 offset:27680
	v_cndmask_b32_e64 v46, v46, 0, vcc
	v_cvt_pk_bf16_f32 v46, v46, v46
	ds_write_b16 v76, v46 offset:36896
	v_sub_f32_e32 v46, v83, v75
	v_min_f32_e32 v46, 0, v46
	v_mul_f32_e32 v46, 0x3fb8aa3b, v46
	v_exp_f32_e32 v46, v46
	v_mul_f32_e32 v50, v79, v51
	v_add3_u32 v77, v77, v86, s81
	ds_write_b16_d16_hi v76, v77 offset:27936
	v_mul_f32_e32 v50, v50, v46
	v_cndmask_b32_e64 v50, v50, 0, vcc
	v_mul_f32_e32 v46, v47, v46
	v_cmp_le_i32_e32 vcc, v34, v70
	v_cvt_pk_bf16_f32 v50, v50, v50
	s_nop 0
	v_cndmask_b32_e32 v46, 0, v46, vcc
	v_cvt_pk_bf16_f32 v46, v46, v46
	ds_write_b16 v76, v46 offset:37040
	v_sub_f32_e32 v46, v84, v75
	v_min_f32_e32 v46, 0, v46
	v_mul_f32_e32 v46, 0x3fb8aa3b, v46
	v_exp_f32_e32 v46, v46
	v_mul_f32_e32 v47, v80, v52
	v_cmp_lt_i32_e32 vcc, v34, v71
	ds_write_b16 v76, v50 offset:27824
	v_mul_f32_e32 v47, v47, v46
	v_cndmask_b32_e32 v47, 0, v47, vcc
	v_mul_f32_e32 v46, v48, v46
	v_cmp_le_i32_e32 vcc, v34, v71
	v_cvt_pk_bf16_f32 v47, v47, v47
	ds_write_b16 v76, v47 offset:27968
	v_cndmask_b32_e32 v46, 0, v46, vcc
	v_cvt_pk_bf16_f32 v46, v46, v46
	ds_write_b16 v76, v46 offset:37184
	v_sub_f32_e32 v46, v85, v75
	v_min_f32_e32 v46, 0, v46
	v_mul_f32_e32 v46, 0x3fb8aa3b, v46
	v_exp_f32_e32 v46, v46
	v_mul_f32_e32 v47, v81, v53
	v_cmp_lt_i32_e32 vcc, v34, v72
	v_bfe_u32 v77, v74, 16, 1
	v_mul_f32_e32 v47, v47, v46
	v_cndmask_b32_e32 v47, 0, v47, vcc
	v_mul_f32_e32 v46, v49, v46
	v_cmp_le_i32_e32 vcc, v34, v72
	v_cvt_pk_bf16_f32 v47, v47, v47
	ds_write_b16 v76, v47 offset:28112
	v_cndmask_b32_e32 v46, 0, v46, vcc
	v_add3_u32 v74, v74, v77, s81
	v_cvt_pk_bf16_f32 v46, v46, v46
	ds_write_b16_d16_hi v76, v74 offset:28080
	ds_write_b16 v76, v46 offset:37328
	v_mov_b32_e32 v33, s84
	ds_read_b128 v[46:49], v33 offset:57600
	ds_read_b128 v[50:53], v33 offset:57616
	s_waitcnt vmcnt(20)
; #define LAS __attribute__((address_space(3)))
; __device__ __forceinline__ unsigned f2bf(float f) { unsigned u = __float_as_uint(f); return (u + 0x7fffu + ((u >> 16) & 1u)) >> 16; }
; __device__ __forceinline__ float gdn_s1(const GdnIn& in, LAS unsigned char* ub, LAS unsigned char* dwb, int w, int lane) {
;     ...
;     { const f32x4 c8a = *(const LAS f32x4*)(GT + 64 + 8 * w), c8b = *(const LAS f32x4*)(GT + 64 + 8 * w + 4);
; #pragma unroll
;       for (int tt = 0; tt < 8; ++tt) KTT[lane * 72 + 8 * w + tt] = (bf16)f2bf(__uint_as_float(in.kt8[tt] << 16) * __expf(cl - (tt < 4 ? c8a[tt & 3] : c8b[tt & 3]))); }
;     asm volatile("s_waitcnt lgkmcnt(0)" ::: "memory");
; __device__ __forceinline__ void gdn_chain_units(CArgs& a, int chain, LAS unsigned char* lds, int w, int lane, unsigned long long& tacc) {
;     ...
;         { gdn_fetch2(a, chain * 36 + n + 1, w, lane, C); const float cl = gdn_s1(B, lds + 27648, dwb, w, lane); __syncthreads(); if (n + 2 < 36) gdn_fetch(a, chain * 36 + n + 2, w, lane, A); gdn_s23(a, chain * 36 + n + 1, C, lds + 27648, dwb, w, lane, cl); }
	v_lshlrev_b32_e32 v55, 16, v137
	v_lshlrev_b32_e32 v54, 16, v135
	v_lshlrev_b32_e32 v57, 16, v133
	s_waitcnt lgkmcnt(1)
	v_sub_f32_e32 v46, s9, v46
	v_sub_f32_e32 v47, s9, v47
	v_sub_f32_e32 v48, s9, v48
	v_sub_f32_e32 v49, s9, v49
	v_mul_f32_e32 v46, 0x3fb8aa3b, v46
	v_mul_f32_e32 v47, 0x3fb8aa3b, v47
	v_mul_f32_e32 v48, 0x3fb8aa3b, v48
	v_mul_f32_e32 v49, 0x3fb8aa3b, v49
	v_exp_f32_e32 v46, v46
	v_exp_f32_e32 v47, v47
	v_exp_f32_e32 v48, v48
	v_exp_f32_e32 v49, v49
	s_waitcnt lgkmcnt(0)
	v_sub_f32_e32 v50, s9, v50
	v_sub_f32_e32 v51, s9, v51
	v_sub_f32_e32 v52, s9, v52
	v_sub_f32_e32 v53, s9, v53
	v_mul_f32_e32 v50, 0x3fb8aa3b, v50
	v_mul_f32_e32 v51, 0x3fb8aa3b, v51
	v_mul_f32_e32 v52, 0x3fb8aa3b, v52
	v_mul_f32_e32 v53, 0x3fb8aa3b, v53
	v_lshlrev_b32_e32 v56, 16, v131
	v_exp_f32_e32 v50, v50
	v_exp_f32_e32 v51, v51
	v_exp_f32_e32 v52, v52
	v_exp_f32_e32 v53, v53
	v_pk_mul_f32 v[46:47], v[46:47], v[56:57]
	v_pk_mul_f32 v[48:49], v[48:49], v[54:55]
	v_bfe_u32 v56, v47, 16, 1
	v_bfe_u32 v54, v49, 16, 1
	v_bfe_u32 v55, v48, 16, 1
	v_bfe_u32 v57, v46, 16, 1
	v_add3_u32 v57, v46, v57, s81
	v_add3_u32 v56, v47, v56, s81
	v_add3_u32 v55, v48, v55, s81
	v_add3_u32 v54, v49, v54, s81
	s_waitcnt vmcnt(16)
	v_lshlrev_b32_e32 v47, 16, v136
	v_lshlrev_b32_e32 v46, 16, v134
	v_lshlrev_b32_e32 v49, 16, v132
	v_lshlrev_b32_e32 v48, 16, v111
	v_pk_mul_f32 v[48:49], v[50:51], v[48:49]
	v_pk_mul_f32 v[46:47], v[52:53], v[46:47]
	v_bfe_u32 v52, v49, 16, 1
	v_bfe_u32 v50, v47, 16, 1
	v_bfe_u32 v51, v46, 16, 1
	v_bfe_u32 v53, v48, 16, 1
	v_mul_lo_u32 v33, v110, s75
	v_add3_u32 v48, v48, v53, s81
	v_add3_u32 v52, v49, v52, s81
	v_add3_u32 v46, v46, v51, s81
	v_add3_u32 v47, v47, v50, s81
	s_mov_b32 s2, 0x7060302
	v_add_u32_e32 v33, s11, v33
	v_perm_b32 v49, v47, v46, s2
	v_perm_b32 v48, v52, v48, s2
	v_perm_b32 v47, v54, v55, s2
	v_perm_b32 v46, v56, v57, s2
	ds_write_b128 v33, v[46:49] offset:46080
	s_waitcnt lgkmcnt(0)
	s_and_b64 vcc, exec, s[50:51]
	s_waitcnt lgkmcnt(0)
	s_barrier
	s_cbranch_vccnz .LBB0_1781
	s_add_i32 s2, s26, 2
	s_mul_hi_i32 s3, s2, 0x38e38e39
	s_lshr_b32 s20, s3, 31
	s_ashr_i32 s3, s3, 3
	s_add_i32 s3, s3, s20
	s_mul_i32 s20, s3, 36
	s_sub_i32 s2, s2, s20
	s_ashr_i32 s36, s3, 3
	s_and_b32 s20, s3, 1
	s_lshl_b32 s29, s2, 6
	s_cmp_gt_i32 s2, 3
	s_mov_b64 s[26:27], -1
	s_cbranch_scc0 .LBB0_1778
	s_add_i32 s2, s29, 0xffffff00
	s_lshl_b32 s26, s36, 11
	s_sub_i32 s27, 0x8ff, s29
	s_cmp_eq_u32 s20, 0
	s_cselect_b32 s2, s2, s27
	s_add_i32 s2, s26, s2
	s_addk_i32 s2, 0x1000
	s_mov_b64 s[26:27], 0

; #define LAS __attribute__((address_space(3)))
; __device__ __forceinline__ unsigned f2bf(float f) { unsigned u = __float_as_uint(f); return (u + 0x7fffu + ((u >> 16) & 1u)) >> 16; }
; __device__ __forceinline__ float lo_bf(unsigned w) { return __uint_as_float(w << 16); }
; __device__ __forceinline__ float hi_bf(unsigned w) { return __uint_as_float(w & 0xffff0000u); }
; __device__ __forceinline__ void gdn_s23(CArgs& a, int u, const GdnIn2& in, LAS unsigned char* ub, LAS unsigned char* dwb, int w, int lane, float cl) {
;     ...
;     { const int blk = lane >> 4, c = lane & 15; float T[16];
; #pragma unroll
;       for (int hb = 0; hb < 4; ++hb) {
;           u32x4 arow[4][2];
; #pragma unroll
;           for (int rr = 0; rr < 4; ++rr) { const int r = 4 * hb + rr; arow[rr][0] = *(const LAS u32x4*)(AB + (16 * blk + r) * 72 + 16 * blk); if (hb >= 2) arow[rr][1] = *(const LAS u32x4*)(AB + (16 * blk + r) * 72 + 16 * blk + 8); }
;           asm volatile("s_waitcnt lgkmcnt(0)" ::: "memory");
; #pragma unroll
;           for (int rr = 0; rr < 4; ++rr) { const int r = 4 * hb + rr; float t = (r == c) ? 1.f : 0.f;
;               float t2 = 0.f;
; #pragma unroll
;               for (int j = 0; j < r; ++j) { const unsigned wv = arow[rr][j >> 3][(j >> 1) & 3]; const float av = (j & 1) ? hi_bf(wv) : lo_bf(wv); if (j & 1) t2 -= av * T[j]; else t -= av * T[j]; }
;               t += t2;
;               T[r] = t; DW[(blk * 16 + r) * 16 + c] = (bf16)f2bf(t); } } }
.LBB0_1781:
	v_and_b32_e32 v76, -16, v110
	v_lshlrev_b32_e32 v34, 1, v106
	v_ashrrev_i32_e32 v82, 4, v110
	v_mov_b32_e32 v225, 1.0
	v_mul_u32_u24_e32 v222, 0x92, v76
	v_lshlrev_b32_e32 v224, 5, v110
	v_and_b32_e32 v224, 0xfffffe00, v224
	v_add3_u32 v223, s8, v34, v224
	v_cmp_eq_u32_e32 vcc, 0, v106
	ds_read_b128 v[46:49], v222 offset:27792
	ds_read_b128 v[54:57], v222 offset:27936
	ds_read_b128 v[62:65], v222 offset:28080
	ds_read_b128 v[70:73], v222 offset:28224
	v_cndmask_b32_e32 v202, 0, v225, vcc
	ds_write_b16_d16_hi v223, v202 offset:55296
	ds_read_b128 v[226:229], v222 offset:28368
	ds_read_b128 v[234:237], v222 offset:28512
	s_waitcnt lgkmcnt(5)
	v_cmp_eq_u32_e32 vcc, 1, v106
	s_nop 1
	v_cndmask_b32_e32 v218, 0, v225, vcc
	v_lshlrev_b32_e32 v220, 16, v46
	v_fma_f32 v203, -v220, v202, v218
	v_cvt_pk_bf16_f32 v224, v203, v203
	ds_write_b16 v223, v224 offset:55328
	v_cmp_eq_u32_e32 vcc, 2, v106
	v_mov_b32_e32 v219, 0
	v_lshlrev_b32_e32 v220, 16, v54
	v_and_b32_e32 v221, 0xffff0000, v54
	v_cndmask_b32_e32 v218, 0, v225, vcc
	v_pk_fma_f32 v[218:219], v[220:221], v[202:203], v[218:219] neg_lo:[1,0,0] neg_hi:[1,0,0]
	v_add_f32_e32 v204, v218, v219
	v_cvt_pk_bf16_f32 v224, v204, v204
	ds_write_b16 v223, v224 offset:55360
	ds_read_b128 v[46:49], v222 offset:28656
	ds_read_b128 v[54:57], v222 offset:28800
	s_waitcnt lgkmcnt(7)
	v_cmp_eq_u32_e32 vcc, 3, v106
	v_mov_b32_e32 v219, 0
	v_lshlrev_b32_e32 v220, 16, v62
	v_and_b32_e32 v221, 0xffff0000, v62
	v_cndmask_b32_e32 v218, 0, v225, vcc
	v_pk_fma_f32 v[218:219], v[220:221], v[202:203], v[218:219] neg_lo:[1,0,0] neg_hi:[1,0,0]
	v_lshlrev_b32_e32 v220, 16, v63
	v_fma_f32 v218, -v220, v204, v218
	v_add_f32_e32 v205, v218, v219
	v_cvt_pk_bf16_f32 v224, v205, v205
	ds_write_b16 v223, v224 offset:55392
	v_cmp_eq_u32_e32 vcc, 4, v106
	v_mov_b32_e32 v219, 0
	v_lshlrev_b32_e32 v220, 16, v70
	v_and_b32_e32 v221, 0xffff0000, v70
	v_cndmask_b32_e32 v218, 0, v225, vcc
	v_pk_fma_f32 v[218:219], v[220:221], v[202:203], v[218:219] neg_lo:[1,0,0] neg_hi:[1,0,0]
	v_lshlrev_b32_e32 v220, 16, v71
	v_and_b32_e32 v221, 0xffff0000, v71
	v_pk_fma_f32 v[218:219], v[220:221], v[204:205], v[218:219] neg_lo:[1,0,0] neg_hi:[1,0,0]
	v_add_f32_e32 v206, v218, v219
	v_cvt_pk_bf16_f32 v224, v206, v206
	ds_write_b16 v223, v224 offset:55424
	ds_read_b128 v[62:65], v222 offset:28944
	ds_read_b128 v[66:69], v222 offset:28960
	ds_read_b128 v[70:73], v222 offset:29088
	ds_read_b128 v[78:81], v222 offset:29104
	s_waitcnt lgkmcnt(10)
	v_cmp_eq_u32_e32 vcc, 5, v106
	v_mov_b32_e32 v219, 0
	v_lshlrev_b32_e32 v220, 16, v226
	v_and_b32_e32 v221, 0xffff0000, v226
	v_cndmask_b32_e32 v218, 0, v225, vcc
	v_pk_fma_f32 v[218:219], v[220:221], v[202:203], v[218:219] neg_lo:[1,0,0] neg_hi:[1,0,0]
	v_lshlrev_b32_e32 v220, 16, v227
	v_and_b32_e32 v221, 0xffff0000, v227
	v_pk_fma_f32 v[218:219], v[220:221], v[204:205], v[218:219] neg_lo:[1,0,0] neg_hi:[1,0,0]
	v_lshlrev_b32_e32 v220, 16, v228
	v_fma_f32 v218, -v220, v206, v218
	v_add_f32_e32 v207, v218, v219
	v_cvt_pk_bf16_f32 v224, v207, v207
	ds_write_b16 v223, v224 offset:55456
	v_cmp_eq_u32_e32 vcc, 6, v106
	v_mov_b32_e32 v219, 0
	v_lshlrev_b32_e32 v220, 16, v234
	v_and_b32_e32 v221, 0xffff0000, v234
	v_cndmask_b32_e32 v218, 0, v225, vcc
	v_pk_fma_f32 v[218:219], v[220:221], v[202:203], v[218:219] neg_lo:[1,0,0] neg_hi:[1,0,0]
	v_lshlrev_b32_e32 v220, 16, v235
	v_and_b32_e32 v221, 0xffff0000, v235
	v_pk_fma_f32 v[218:219], v[220:221], v[204:205], v[218:219] neg_lo:[1,0,0] neg_hi:[1,0,0]
	v_lshlrev_b32_e32 v220, 16, v236
	v_and_b32_e32 v221, 0xffff0000, v236
	v_pk_fma_f32 v[218:219], v[220:221], v[206:207], v[218:219] neg_lo:[1,0,0] neg_hi:[1,0,0]
	v_add_f32_e32 v208, v218, v219
	v_cvt_pk_bf16_f32 v224, v208, v208
	ds_write_b16 v223, v224 offset:55488
	ds_read_b128 v[226:229], v222 offset:29232
	ds_read_b128 v[230:233], v222 offset:29248
	ds_read_b128 v[234:237], v222 offset:29376
	ds_read_b128 v[238:241], v222 offset:29392
	s_waitcnt lgkmcnt(12)
	v_cmp_eq_u32_e32 vcc, 7, v106
	v_mov_b32_e32 v219, 0
	v_lshlrev_b32_e32 v220, 16, v46
	v_and_b32_e32 v221, 0xffff0000, v46
	v_cndmask_b32_e32 v218, 0, v225, vcc
	v_pk_fma_f32 v[218:219], v[220:221], v[202:203], v[218:219] neg_lo:[1,0,0] neg_hi:[1,0,0]
	v_lshlrev_b32_e32 v220, 16, v47
	v_and_b32_e32 v221, 0xffff0000, v47
	v_pk_fma_f32 v[218:219], v[220:221], v[204:205], v[218:219] neg_lo:[1,0,0] neg_hi:[1,0,0]
	v_lshlrev_b32_e32 v220, 16, v48
	v_and_b32_e32 v221, 0xffff0000, v48
	v_pk_fma_f32 v[218:219], v[220:221], v[206:207], v[218:219] neg_lo:[1,0,0] neg_hi:[1,0,0]
	v_lshlrev_b32_e32 v220, 16, v49
	v_fma_f32 v218, -v220, v208, v218
	v_add_f32_e32 v209, v218, v219
	v_cvt_pk_bf16_f32 v224, v209, v209
	ds_write_b16 v223, v224 offset:55520
	v_cmp_eq_u32_e32 vcc, 8, v106
	v_mov_b32_e32 v219, 0
	v_lshlrev_b32_e32 v220, 16, v54
	v_and_b32_e32 v221, 0xffff0000, v54
	v_cndmask_b32_e32 v218, 0, v225, vcc
	v_pk_fma_f32 v[218:219], v[220:221], v[202:203], v[218:219] neg_lo:[1,0,0] neg_hi:[1,0,0]
	v_lshlrev_b32_e32 v220, 16, v55
	v_and_b32_e32 v221, 0xffff0000, v55
	v_pk_fma_f32 v[218:219], v[220:221], v[204:205], v[218:219] neg_lo:[1,0,0] neg_hi:[1,0,0]
	v_lshlrev_b32_e32 v220, 16, v56
	v_and_b32_e32 v221, 0xffff0000, v56
	v_pk_fma_f32 v[218:219], v[220:221], v[206:207], v[218:219] neg_lo:[1,0,0] neg_hi:[1,0,0]
	v_lshlrev_b32_e32 v220, 16, v57
	v_and_b32_e32 v221, 0xffff0000, v57
	v_pk_fma_f32 v[218:219], v[220:221], v[208:209], v[218:219] neg_lo:[1,0,0] neg_hi:[1,0,0]
	v_add_f32_e32 v210, v218, v219
	v_cvt_pk_bf16_f32 v224, v210, v210
	ds_write_b16 v223, v224 offset:55552
	ds_read_b128 v[46:49], v222 offset:29520
	ds_read_b128 v[50:53], v222 offset:29536
	ds_read_b128 v[54:57], v222 offset:29664
	ds_read_b128 v[58:61], v222 offset:29680
	s_waitcnt lgkmcnt(12)
; #define LAS __attribute__((address_space(3)))
; __device__ __forceinline__ unsigned f2bf(float f) { unsigned u = __float_as_uint(f); return (u + 0x7fffu + ((u >> 16) & 1u)) >> 16; }
; __device__ __forceinline__ float lo_bf(unsigned w) { return __uint_as_float(w << 16); }
; __device__ __forceinline__ float hi_bf(unsigned w) { return __uint_as_float(w & 0xffff0000u); }
; __device__ __forceinline__ void gdn_s23(CArgs& a, int u, const GdnIn2& in, LAS unsigned char* ub, LAS unsigned char* dwb, int w, int lane, float cl) {
;     ...
;     { const int blk = lane >> 4, c = lane & 15; float T[16];
; #pragma unroll
;       for (int hb = 0; hb < 4; ++hb) {
;           u32x4 arow[4][2];
; #pragma unroll
;           for (int rr = 0; rr < 4; ++rr) { const int r = 4 * hb + rr; arow[rr][0] = *(const LAS u32x4*)(AB + (16 * blk + r) * 72 + 16 * blk); if (hb >= 2) arow[rr][1] = *(const LAS u32x4*)(AB + (16 * blk + r) * 72 + 16 * blk + 8); }
;           asm volatile("s_waitcnt lgkmcnt(0)" ::: "memory");
; #pragma unroll
;           for (int rr = 0; rr < 4; ++rr) { const int r = 4 * hb + rr; float t = (r == c) ? 1.f : 0.f;
;               float t2 = 0.f;
; #pragma unroll
;               for (int j = 0; j < r; ++j) { const unsigned wv = arow[rr][j >> 3][(j >> 1) & 3]; const float av = (j & 1) ? hi_bf(wv) : lo_bf(wv); if (j & 1) t2 -= av * T[j]; else t -= av * T[j]; }
;               t += t2;
;               T[r] = t; DW[(blk * 16 + r) * 16 + c] = (bf16)f2bf(t); } } }
	v_cmp_eq_u32_e32 vcc, 9, v106
	v_mov_b32_e32 v219, 0
	v_lshlrev_b32_e32 v220, 16, v62
	v_and_b32_e32 v221, 0xffff0000, v62
	v_cndmask_b32_e32 v218, 0, v225, vcc
	v_pk_fma_f32 v[218:219], v[220:221], v[202:203], v[218:219] neg_lo:[1,0,0] neg_hi:[1,0,0]
	v_lshlrev_b32_e32 v220, 16, v63
	v_and_b32_e32 v221, 0xffff0000, v63
	v_pk_fma_f32 v[218:219], v[220:221], v[204:205], v[218:219] neg_lo:[1,0,0] neg_hi:[1,0,0]
	v_lshlrev_b32_e32 v220, 16, v64
	v_and_b32_e32 v221, 0xffff0000, v64
	v_pk_fma_f32 v[218:219], v[220:221], v[206:207], v[218:219] neg_lo:[1,0,0] neg_hi:[1,0,0]
	v_lshlrev_b32_e32 v220, 16, v65
	v_and_b32_e32 v221, 0xffff0000, v65
	v_pk_fma_f32 v[218:219], v[220:221], v[208:209], v[218:219] neg_lo:[1,0,0] neg_hi:[1,0,0]
	v_lshlrev_b32_e32 v220, 16, v66
	v_fma_f32 v218, -v220, v210, v218
	v_add_f32_e32 v211, v218, v219
	v_cvt_pk_bf16_f32 v224, v211, v211
	ds_write_b16 v223, v224 offset:55584
	v_cmp_eq_u32_e32 vcc, 10, v106
	v_mov_b32_e32 v219, 0
	v_lshlrev_b32_e32 v220, 16, v70
	v_and_b32_e32 v221, 0xffff0000, v70
	v_cndmask_b32_e32 v218, 0, v225, vcc
	v_pk_fma_f32 v[218:219], v[220:221], v[202:203], v[218:219] neg_lo:[1,0,0] neg_hi:[1,0,0]
	v_lshlrev_b32_e32 v220, 16, v71
	v_and_b32_e32 v221, 0xffff0000, v71
	v_pk_fma_f32 v[218:219], v[220:221], v[204:205], v[218:219] neg_lo:[1,0,0] neg_hi:[1,0,0]
	v_lshlrev_b32_e32 v220, 16, v72
	v_and_b32_e32 v221, 0xffff0000, v72
	v_pk_fma_f32 v[218:219], v[220:221], v[206:207], v[218:219] neg_lo:[1,0,0] neg_hi:[1,0,0]
	v_lshlrev_b32_e32 v220, 16, v73
	v_and_b32_e32 v221, 0xffff0000, v73
	v_pk_fma_f32 v[218:219], v[220:221], v[208:209], v[218:219] neg_lo:[1,0,0] neg_hi:[1,0,0]
	v_lshlrev_b32_e32 v220, 16, v78
	v_and_b32_e32 v221, 0xffff0000, v78
	v_pk_fma_f32 v[218:219], v[220:221], v[210:211], v[218:219] neg_lo:[1,0,0] neg_hi:[1,0,0]
	v_add_f32_e32 v212, v218, v219
	v_cvt_pk_bf16_f32 v224, v212, v212
	ds_write_b16 v223, v224 offset:55616
	ds_read_b128 v[62:65], v222 offset:29808
	ds_read_b128 v[66:69], v222 offset:29824
	s_waitcnt lgkmcnt(10)
	v_cmp_eq_u32_e32 vcc, 11, v106
	v_mov_b32_e32 v219, 0
	v_lshlrev_b32_e32 v220, 16, v226
	v_and_b32_e32 v221, 0xffff0000, v226
	v_cndmask_b32_e32 v218, 0, v225, vcc
	v_pk_fma_f32 v[218:219], v[220:221], v[202:203], v[218:219] neg_lo:[1,0,0] neg_hi:[1,0,0]
	v_lshlrev_b32_e32 v220, 16, v227
	v_and_b32_e32 v221, 0xffff0000, v227
	v_pk_fma_f32 v[218:219], v[220:221], v[204:205], v[218:219] neg_lo:[1,0,0] neg_hi:[1,0,0]
	v_lshlrev_b32_e32 v220, 16, v228
	v_and_b32_e32 v221, 0xffff0000, v228
	v_pk_fma_f32 v[218:219], v[220:221], v[206:207], v[218:219] neg_lo:[1,0,0] neg_hi:[1,0,0]
	v_lshlrev_b32_e32 v220, 16, v229
	v_and_b32_e32 v221, 0xffff0000, v229
	v_pk_fma_f32 v[218:219], v[220:221], v[208:209], v[218:219] neg_lo:[1,0,0] neg_hi:[1,0,0]
	v_lshlrev_b32_e32 v220, 16, v230
	v_and_b32_e32 v221, 0xffff0000, v230
	v_pk_fma_f32 v[218:219], v[220:221], v[210:211], v[218:219] neg_lo:[1,0,0] neg_hi:[1,0,0]
	v_lshlrev_b32_e32 v220, 16, v231
	v_fma_f32 v218, -v220, v212, v218
	v_add_f32_e32 v213, v218, v219
	v_cvt_pk_bf16_f32 v224, v213, v213
	ds_write_b16 v223, v224 offset:55648
	v_cmp_eq_u32_e32 vcc, 12, v106
	v_mov_b32_e32 v219, 0
	v_lshlrev_b32_e32 v220, 16, v234
	v_and_b32_e32 v221, 0xffff0000, v234
	v_cndmask_b32_e32 v218, 0, v225, vcc
	v_pk_fma_f32 v[218:219], v[220:221], v[202:203], v[218:219] neg_lo:[1,0,0] neg_hi:[1,0,0]
	v_lshlrev_b32_e32 v220, 16, v235
	v_and_b32_e32 v221, 0xffff0000, v235
	v_pk_fma_f32 v[218:219], v[220:221], v[204:205], v[218:219] neg_lo:[1,0,0] neg_hi:[1,0,0]
	v_lshlrev_b32_e32 v220, 16, v236
	v_and_b32_e32 v221, 0xffff0000, v236
	v_pk_fma_f32 v[218:219], v[220:221], v[206:207], v[218:219] neg_lo:[1,0,0] neg_hi:[1,0,0]
	v_lshlrev_b32_e32 v220, 16, v237
	v_and_b32_e32 v221, 0xffff0000, v237
	v_pk_fma_f32 v[218:219], v[220:221], v[208:209], v[218:219] neg_lo:[1,0,0] neg_hi:[1,0,0]
	v_lshlrev_b32_e32 v220, 16, v238
	v_and_b32_e32 v221, 0xffff0000, v238
	v_pk_fma_f32 v[218:219], v[220:221], v[210:211], v[218:219] neg_lo:[1,0,0] neg_hi:[1,0,0]
	v_lshlrev_b32_e32 v220, 16, v239
	v_and_b32_e32 v221, 0xffff0000, v239
	v_pk_fma_f32 v[218:219], v[220:221], v[212:213], v[218:219] neg_lo:[1,0,0] neg_hi:[1,0,0]
	v_add_f32_e32 v214, v218, v219
	v_cvt_pk_bf16_f32 v224, v214, v214
	ds_write_b16 v223, v224 offset:55680
	s_waitcnt lgkmcnt(6)
; #define LAS __attribute__((address_space(3)))
; __device__ __forceinline__ unsigned f2bf(float f) { unsigned u = __float_as_uint(f); return (u + 0x7fffu + ((u >> 16) & 1u)) >> 16; }
; __device__ __forceinline__ float lo_bf(unsigned w) { return __uint_as_float(w << 16); }
; __device__ __forceinline__ float hi_bf(unsigned w) { return __uint_as_float(w & 0xffff0000u); }
; __device__ __forceinline__ void gdn_s23(CArgs& a, int u, const GdnIn2& in, LAS unsigned char* ub, LAS unsigned char* dwb, int w, int lane, float cl) {
;     ...
;     { const int blk = lane >> 4, c = lane & 15; float T[16];
; #pragma unroll
;       for (int hb = 0; hb < 4; ++hb) {
;           u32x4 arow[4][2];
; #pragma unroll
;           for (int rr = 0; rr < 4; ++rr) { const int r = 4 * hb + rr; arow[rr][0] = *(const LAS u32x4*)(AB + (16 * blk + r) * 72 + 16 * blk); if (hb >= 2) arow[rr][1] = *(const LAS u32x4*)(AB + (16 * blk + r) * 72 + 16 * blk + 8); }
;           asm volatile("s_waitcnt lgkmcnt(0)" ::: "memory");
; #pragma unroll
;           for (int rr = 0; rr < 4; ++rr) { const int r = 4 * hb + rr; float t = (r == c) ? 1.f : 0.f;
;               float t2 = 0.f;
; #pragma unroll
;               for (int j = 0; j < r; ++j) { const unsigned wv = arow[rr][j >> 3][(j >> 1) & 3]; const float av = (j & 1) ? hi_bf(wv) : lo_bf(wv); if (j & 1) t2 -= av * T[j]; else t -= av * T[j]; }
;               t += t2;
;               T[r] = t; DW[(blk * 16 + r) * 16 + c] = (bf16)f2bf(t); } } }
; __device__ __forceinline__ void gdn_chain_units(CArgs& a, int chain, LAS unsigned char* lds, int w, int lane, unsigned long long& tacc) {
;     ...
;         { gdn_fetch2(a, chain * 36 + n + 1, w, lane, C); const float cl = gdn_s1(B, lds + 27648, dwb, w, lane); __syncthreads(); if (n + 2 < 36) gdn_fetch(a, chain * 36 + n + 2, w, lane, A); gdn_s23(a, chain * 36 + n + 1, C, lds + 27648, dwb, w, lane, cl); }
	v_cmp_eq_u32_e32 vcc, 13, v106
	v_mov_b32_e32 v219, 0
	v_lshlrev_b32_e32 v220, 16, v46
	v_and_b32_e32 v221, 0xffff0000, v46
	v_cndmask_b32_e32 v218, 0, v225, vcc
	v_pk_fma_f32 v[218:219], v[220:221], v[202:203], v[218:219] neg_lo:[1,0,0] neg_hi:[1,0,0]
	v_lshlrev_b32_e32 v220, 16, v47
	v_and_b32_e32 v221, 0xffff0000, v47
	v_pk_fma_f32 v[218:219], v[220:221], v[204:205], v[218:219] neg_lo:[1,0,0] neg_hi:[1,0,0]
	v_lshlrev_b32_e32 v220, 16, v48
	v_and_b32_e32 v221, 0xffff0000, v48
	v_pk_fma_f32 v[218:219], v[220:221], v[206:207], v[218:219] neg_lo:[1,0,0] neg_hi:[1,0,0]
	v_lshlrev_b32_e32 v220, 16, v49
	v_and_b32_e32 v221, 0xffff0000, v49
	v_pk_fma_f32 v[218:219], v[220:221], v[208:209], v[218:219] neg_lo:[1,0,0] neg_hi:[1,0,0]
	v_lshlrev_b32_e32 v220, 16, v50
	v_and_b32_e32 v221, 0xffff0000, v50
	v_pk_fma_f32 v[218:219], v[220:221], v[210:211], v[218:219] neg_lo:[1,0,0] neg_hi:[1,0,0]
	v_lshlrev_b32_e32 v220, 16, v51
	v_and_b32_e32 v221, 0xffff0000, v51
	v_pk_fma_f32 v[218:219], v[220:221], v[212:213], v[218:219] neg_lo:[1,0,0] neg_hi:[1,0,0]
	v_lshlrev_b32_e32 v220, 16, v52
	v_fma_f32 v218, -v220, v214, v218
	v_add_f32_e32 v215, v218, v219
	v_cvt_pk_bf16_f32 v224, v215, v215
	ds_write_b16 v223, v224 offset:55712
	v_cmp_eq_u32_e32 vcc, 14, v106
	v_mov_b32_e32 v219, 0
	v_lshlrev_b32_e32 v220, 16, v54
	v_and_b32_e32 v221, 0xffff0000, v54
	v_cndmask_b32_e32 v218, 0, v225, vcc
	v_pk_fma_f32 v[218:219], v[220:221], v[202:203], v[218:219] neg_lo:[1,0,0] neg_hi:[1,0,0]
	v_lshlrev_b32_e32 v220, 16, v55
	v_and_b32_e32 v221, 0xffff0000, v55
	v_pk_fma_f32 v[218:219], v[220:221], v[204:205], v[218:219] neg_lo:[1,0,0] neg_hi:[1,0,0]
	v_lshlrev_b32_e32 v220, 16, v56
	v_and_b32_e32 v221, 0xffff0000, v56
	v_pk_fma_f32 v[218:219], v[220:221], v[206:207], v[218:219] neg_lo:[1,0,0] neg_hi:[1,0,0]
	v_lshlrev_b32_e32 v220, 16, v57
	v_and_b32_e32 v221, 0xffff0000, v57
	v_pk_fma_f32 v[218:219], v[220:221], v[208:209], v[218:219] neg_lo:[1,0,0] neg_hi:[1,0,0]
	v_lshlrev_b32_e32 v220, 16, v58
	v_and_b32_e32 v221, 0xffff0000, v58
	v_pk_fma_f32 v[218:219], v[220:221], v[210:211], v[218:219] neg_lo:[1,0,0] neg_hi:[1,0,0]
	v_lshlrev_b32_e32 v220, 16, v59
	v_and_b32_e32 v221, 0xffff0000, v59
	v_pk_fma_f32 v[218:219], v[220:221], v[212:213], v[218:219] neg_lo:[1,0,0] neg_hi:[1,0,0]
	v_lshlrev_b32_e32 v220, 16, v60
	v_and_b32_e32 v221, 0xffff0000, v60
	v_pk_fma_f32 v[218:219], v[220:221], v[214:215], v[218:219] neg_lo:[1,0,0] neg_hi:[1,0,0]
	v_add_f32_e32 v216, v218, v219
	v_cvt_pk_bf16_f32 v224, v216, v216
	ds_write_b16 v223, v224 offset:55744
	s_waitcnt lgkmcnt(4)
	v_cmp_eq_u32_e32 vcc, 15, v106
	v_mov_b32_e32 v219, 0
	v_lshlrev_b32_e32 v220, 16, v62
	v_and_b32_e32 v221, 0xffff0000, v62
	v_cndmask_b32_e32 v218, 0, v225, vcc
	v_pk_fma_f32 v[218:219], v[220:221], v[202:203], v[218:219] neg_lo:[1,0,0] neg_hi:[1,0,0]
	v_lshlrev_b32_e32 v220, 16, v63
	v_and_b32_e32 v221, 0xffff0000, v63
	v_pk_fma_f32 v[218:219], v[220:221], v[204:205], v[218:219] neg_lo:[1,0,0] neg_hi:[1,0,0]
	v_lshlrev_b32_e32 v220, 16, v64
	v_and_b32_e32 v221, 0xffff0000, v64
	v_pk_fma_f32 v[218:219], v[220:221], v[206:207], v[218:219] neg_lo:[1,0,0] neg_hi:[1,0,0]
	v_lshlrev_b32_e32 v220, 16, v65
	v_and_b32_e32 v221, 0xffff0000, v65
	v_pk_fma_f32 v[218:219], v[220:221], v[208:209], v[218:219] neg_lo:[1,0,0] neg_hi:[1,0,0]
	v_lshlrev_b32_e32 v220, 16, v66
	v_and_b32_e32 v221, 0xffff0000, v66
	v_pk_fma_f32 v[218:219], v[220:221], v[210:211], v[218:219] neg_lo:[1,0,0] neg_hi:[1,0,0]
	v_lshlrev_b32_e32 v220, 16, v67
	v_and_b32_e32 v221, 0xffff0000, v67
	v_pk_fma_f32 v[218:219], v[220:221], v[212:213], v[218:219] neg_lo:[1,0,0] neg_hi:[1,0,0]
	v_lshlrev_b32_e32 v220, 16, v68
	v_and_b32_e32 v221, 0xffff0000, v68
	v_pk_fma_f32 v[218:219], v[220:221], v[214:215], v[218:219] neg_lo:[1,0,0] neg_hi:[1,0,0]
	v_lshlrev_b32_e32 v220, 16, v69
	v_fma_f32 v218, -v220, v216, v218
	v_add_f32_e32 v217, v218, v219
	v_cvt_pk_bf16_f32 v224, v217, v217
	ds_write_b16 v223, v224 offset:55776
	s_and_b64 vcc, exec, s[50:51]
	s_cbranch_vccnz .Lgdf_last
	s_waitcnt vmcnt(17)
	s_branch .Lgdf_j

; #define LAS __attribute__((address_space(3)))
; __device__ __forceinline__ u32x2 cvt4(f32x4 v) { return (u32x2){pk2(v[0], v[1]), pk2(v[2], v[3])}; }
; __device__ __forceinline__ void gdn_s23(CArgs& a, int u, const GdnIn2& in, LAS unsigned char* ub, LAS unsigned char* dwb, int w, int lane, float cl) {
;     ...
;     asm volatile("s_waitcnt lgkmcnt(0)" ::: "memory");
;     f32x4 X[4];
; #pragma unroll
;     for (int I = 0; I < 4; ++I) {
;         const f32x4 br = *(const LAS f32x4*)(GT + 16 * I + 4 * kg), er = *(const LAS f32x4*)(GT + 128 + 16 * I + 4 * kg);
;         const f32x4 Rf = (f32x4){__uint_as_float(in.R[I].x << 16), __uint_as_float(in.R[I].y << 16), __uint_as_float(in.R[I].z << 16), __uint_as_float(in.R[I].w << 16)};
;         f32x4 acc = isW ? br * er * Rf : br * Rf;
; #pragma unroll
;         for (int P = 0; 2 * P < I; ++P) {
;             const u32x2 alo = *(const LAS u32x2*)(AB + (16 * I + fr) * 72 + 32 * P + 4 * kg);
;             const u32x2 ahi = (2 * P + 1 < I) ? *(const LAS u32x2*)(AB + (16 * I + fr) * 72 + 32 * P + 16 + 4 * kg) : (u32x2){0u, 0u};
;             const u32x2 xlo = cvt4(-X[2 * P]); const u32x2 xhi = (2 * P + 1 < I) ? cvt4(-X[2 * P + 1]) : (u32x2){0u, 0u};
;             acc = __builtin_amdgcn_mfma_f32_16x16x32_bf16(frag2(alo, ahi), frag2(xlo, xhi), acc, 0, 0, 0); }
;         const u32x2 dlo = *(const LAS u32x2*)(DW + (I * 16 + fr) * 16 + 4 * kg);
;         X[I] = __builtin_amdgcn_mfma_f32_16x16x32_bf16(frag2(dlo, (u32x2){0u, 0u}), frag2(cvt4(acc), (u32x2){0u, 0u}), (f32x4){0.f, 0.f, 0.f, 0.f}, 0, 0, 0);
;     }
.Lgdf_j:
	v_lshlrev_b32_e32 v103, 16, v103
	v_lshlrev_b32_e32 v102, 16, v102
	v_lshlrev_b32_e32 v105, 16, v105
	v_lshlrev_b32_e32 v104, 16, v104
	v_lshlrev_b32_e32 v99, 16, v99
	v_lshlrev_b32_e32 v98, 16, v98
	v_lshlrev_b32_e32 v101, 16, v101
	v_lshlrev_b32_e32 v100, 16, v100
	v_lshlrev_b32_e32 v96, 16, v96
	v_lshlrev_b32_e32 v94, 16, v94
	v_lshlrev_b32_e32 v97, 16, v97
	v_lshlrev_b32_e32 v95, 16, v95
	v_lshlrev_b32_e32 v92, 16, v92
	v_lshlrev_b32_e32 v90, 16, v90
	v_lshlrev_b32_e32 v93, 16, v93
	v_lshlrev_b32_e32 v91, 16, v91
	s_waitcnt lgkmcnt(0)
	v_add_u32_e32 v79, s8, v76
	ds_read_b128 v[46:49], v79 offset:57344
	ds_read_b128 v[54:57], v79 offset:57856
	v_lshlrev_b32_e32 v70, 3, v82
	v_sub_u32_e32 v33, v79, v70
	s_waitcnt vmcnt(15)
	v_lshlrev_b32_e32 v50, 16, v123
	s_waitcnt vmcnt(14)
	v_lshlrev_b32_e32 v51, 16, v139
	s_waitcnt lgkmcnt(0)
	v_pk_mul_f32 v[60:61], v[46:47], v[54:55]
	v_pk_mul_f32 v[58:59], v[48:49], v[56:57]
	v_cndmask_b32_e64 v47, v47, v61, s[38:39]
	v_cndmask_b32_e64 v46, v46, v60, s[38:39]
	v_pk_mul_f32 v[50:51], v[46:47], v[50:51]
	v_lshl_add_u32 v46, v106, 5, v33
	ds_read_b64 v[46:47], v46 offset:55296
	v_cndmask_b32_e64 v48, v48, v58, s[38:39]
	s_waitcnt vmcnt(13)
	v_lshlrev_b32_e32 v52, 16, v141
	s_waitcnt vmcnt(12)
	v_lshlrev_b32_e32 v53, 16, v142
	v_cndmask_b32_e64 v49, v49, v59, s[38:39]
	v_pk_mul_f32 v[52:53], v[48:49], v[52:53]
	v_mov_b32_e32 v48, v35
	v_mov_b32_e32 v49, v35
	v_cvt_pk_bf16_f32 v50, v50, v51
	v_cvt_pk_bf16_f32 v51, v52, v53
	v_mov_b32_e32 v52, v35
	v_mov_b32_e32 v53, v35
	s_waitcnt vmcnt(9)
	v_lshlrev_b32_e32 v60, 16, v138
	s_waitcnt vmcnt(8)
	v_lshlrev_b32_e32 v61, 16, v140
	s_waitcnt lgkmcnt(0)
	v_mfma_f32_16x16x32_bf16 v[62:65], v[46:49], v[50:53], 0
	ds_read_b128 v[46:49], v79 offset:57408
	ds_read_b128 v[50:53], v79 offset:57920
	v_or_b32_e32 v89, 16, v106
	v_add_u32_e32 v86, 0, v70
	v_lshlrev_b32_e32 v58, 16, v121
	v_lshlrev_b32_e32 v59, 16, v122
	s_waitcnt lgkmcnt(0)
	v_pk_mul_f32 v[66:67], v[48:49], v[52:53]
	v_pk_mul_f32 v[68:69], v[46:47], v[50:51]
	v_cndmask_b32_e64 v49, v49, v67, s[38:39]
	v_xor_b32_e32 v67, 0x80000000, v63
	v_cndmask_b32_e64 v48, v48, v66, s[38:39]
	v_cndmask_b32_e64 v46, v46, v68, s[38:39]
	v_xor_b32_e32 v66, 0x80000000, v62
	v_bfe_u32 v68, v67, 16, 1
	v_add3_u32 v67, v67, v68, s81
	v_bfe_u32 v68, v66, 16, 1
	v_add3_u32 v66, v66, v68, s81
	v_cndmask_b32_e64 v47, v47, v69, s[38:39]
	v_pk_mul_f32 v[48:49], v[48:49], v[60:61]
	v_mad_u32_u24 v78, v89, s75, v86
	v_xor_b32_e32 v61, 0x80000000, v65
	v_lshrrev_b32_e32 v66, 16, v66
	v_pk_mul_f32 v[46:47], v[46:47], v[58:59]
	ds_read_b64 v[58:59], v78 offset:27648
	v_xor_b32_e32 v60, 0x80000000, v64
	v_and_or_b32 v74, v67, s80, v66
	v_cvt_pk_bf16_f32 v75, v60, v61
	v_mov_b32_e32 v60, v35
	v_mov_b32_e32 v61, v35
	v_mov_b32_e32 v76, v35
	v_mov_b32_e32 v77, v35
	s_waitcnt vmcnt(7)
	v_lshlrev_b32_e32 v70, 16, v107
	s_waitcnt vmcnt(6)
	v_lshlrev_b32_e32 v71, 16, v108
	s_waitcnt lgkmcnt(0)
	v_mfma_f32_16x16x32_bf16 v[46:49], v[58:61], v[74:77], v[46:49]
	v_lshl_add_u32 v58, v89, 5, v33
	ds_read_b64 v[58:59], v58 offset:55296
	s_waitcnt vmcnt(5)
	v_lshlrev_b32_e32 v72, 16, v109
	s_waitcnt vmcnt(4)
	v_lshlrev_b32_e32 v73, 16, v117
	v_or_b32_e32 v88, 32, v106
	s_nop 0
	v_cvt_pk_bf16_f32 v46, v46, v46
	v_bfe_u32 v66, v47, 16, 1
	v_lshrrev_b32_e32 v46, 16, v46
	v_add3_u32 v47, v47, v66, s81
	v_and_or_b32 v46, v47, s80, v46
	v_cvt_pk_bf16_f32 v47, v48, v49
	v_mov_b32_e32 v48, v35
	v_mov_b32_e32 v49, v35
	s_waitcnt vmcnt(1)
	v_lshlrev_b32_e32 v84, 16, v119
	s_waitcnt vmcnt(0)
	v_lshlrev_b32_e32 v85, 16, v120
	s_waitcnt lgkmcnt(0)
	v_mfma_f32_16x16x32_bf16 v[66:69], v[58:61], v[46:49], 0
	ds_read_b128 v[46:49], v79 offset:57472
	ds_read_b128 v[58:61], v79 offset:57984
	v_or_b32_e32 v87, 48, v106
	s_ashr_i32 s29, s28, 31
	s_lshl_b64 s[52:53], s[28:29], 13
	s_add_u32 s26, s85, s52
	s_waitcnt lgkmcnt(0)
; #define LAS __attribute__((address_space(3)))
; __device__ __forceinline__ u32x2 cvt4(f32x4 v) { return (u32x2){pk2(v[0], v[1]), pk2(v[2], v[3])}; }
; __device__ __forceinline__ void gdn_s23(CArgs& a, int u, const GdnIn2& in, LAS unsigned char* ub, LAS unsigned char* dwb, int w, int lane, float cl) {
;     ...
; #pragma unroll
;         for (int P = 0; 2 * P < I; ++P) {
;             const u32x2 alo = *(const LAS u32x2*)(AB + (16 * I + fr) * 72 + 32 * P + 4 * kg);
;             const u32x2 ahi = (2 * P + 1 < I) ? *(const LAS u32x2*)(AB + (16 * I + fr) * 72 + 32 * P + 16 + 4 * kg) : (u32x2){0u, 0u};
;             const u32x2 xlo = cvt4(-X[2 * P]); const u32x2 xhi = (2 * P + 1 < I) ? cvt4(-X[2 * P + 1]) : (u32x2){0u, 0u};
;             acc = __builtin_amdgcn_mfma_f32_16x16x32_bf16(frag2(alo, ahi), frag2(xlo, xhi), acc, 0, 0, 0); }
;         const u32x2 dlo = *(const LAS u32x2*)(DW + (I * 16 + fr) * 16 + 4 * kg);
;         X[I] = __builtin_amdgcn_mfma_f32_16x16x32_bf16(frag2(dlo, (u32x2){0u, 0u}), frag2(cvt4(acc), (u32x2){0u, 0u}), (f32x4){0.f, 0.f, 0.f, 0.f}, 0, 0, 0);
;     }
;     const bf16x8 Xb01 = frag2(cvt4(X[0]), cvt4(X[1])), Xb23 = frag2(cvt4(X[2]), cvt4(X[3]));
;     const float ecl = __expf(cl);
;     bf16* ftp = FTo + (c0 + fr) * 64 + 4 * kg; bf16* btp = BTo + (c0 + fr) * 64 + 4 * kg; bf16* ep = Eo + (4 * kg) * 64 + c0 + fr; bf16* mp = Mo + (4 * kg) * 64 + c0 + fr;
; #pragma unroll
;     for (int t4 = 0; t4 < 4; ++t4) {
;         const LAS bf16* ar = ATT + (16 * t4 + fr) * 72 + 4 * kg; const LAS bf16* kr = KTT + (16 * t4 + fr) * 72 + 4 * kg;
;         f32x4 pa = (f32x4){0.f, 0.f, 0.f, 0.f}, pk = (f32x4){0.f, 0.f, 0.f, 0.f};
;         pa = __builtin_amdgcn_mfma_f32_16x16x32_bf16(frag2(*(const LAS u32x2*)ar, *(const LAS u32x2*)(ar + 16)), Xb01, pa, 0, 0, 0);
;         pa = __builtin_amdgcn_mfma_f32_16x16x32_bf16(frag2(*(const LAS u32x2*)(ar + 32), *(const LAS u32x2*)(ar + 48)), Xb23, pa, 0, 0, 0);
;         pk = __builtin_amdgcn_mfma_f32_16x16x32_bf16(frag2(*(const LAS u32x2*)kr, *(const LAS u32x2*)(kr + 16)), Xb01, pk, 0, 0, 0);
;         pk = __builtin_amdgcn_mfma_f32_16x16x32_bf16(frag2(*(const LAS u32x2*)(kr + 32), *(const LAS u32x2*)(kr + 48)), Xb23, pk, 0, 0, 0);
;         if (!isW) {
;             *(u32x2*)(ftp + 16 * t4) = cvt4(pa);
;             *(u32x2*)(btp + 16 * t4) = cvt4(pk);
	v_pk_mul_f32 v[80:81], v[46:47], v[58:59]
	v_pk_mul_f32 v[76:77], v[48:49], v[60:61]
	v_cndmask_b32_e64 v47, v47, v81, s[38:39]
	v_cndmask_b32_e64 v46, v46, v80, s[38:39]
	v_cndmask_b32_e64 v49, v49, v77, s[38:39]
	v_cndmask_b32_e64 v48, v48, v76, s[38:39]
	v_pk_mul_f32 v[46:47], v[46:47], v[70:71]
	v_add_u32_e32 v70, 0x7000, v78
	v_xor_b32_e32 v81, 0x80000000, v67
	v_pk_mul_f32 v[48:49], v[48:49], v[72:73]
	ds_read2_b64 v[70:73], v70 offset0:160 offset1:164
	v_xor_b32_e32 v76, 0x80000000, v66
	v_xor_b32_e32 v80, 0x80000000, v69
	v_xor_b32_e32 v77, 0x80000000, v68
	v_cvt_pk_bf16_f32 v76, v76, v81
	v_cvt_pk_bf16_f32 v77, v77, v80
	v_lshlrev_b32_e32 v81, 16, v118
	s_addc_u32 s27, s64, s53
	s_waitcnt lgkmcnt(0)
	v_mfma_f32_16x16x32_bf16 v[46:49], v[70:73], v[74:77], v[46:49]
	v_lshl_add_u32 v70, v88, 5, v33
	ds_read_b64 v[70:71], v70 offset:55296
	v_mov_b32_e32 v72, v35
	v_mov_b32_e32 v73, v35
	v_lshl_add_u32 v33, v87, 5, v33
	s_nop 2
	v_cvt_pk_bf16_f32 v46, v46, v47
	v_cvt_pk_bf16_f32 v47, v48, v49
	v_mov_b32_e32 v48, v35
	v_mov_b32_e32 v49, v35
	v_lshlrev_b32_e32 v80, 16, v116
	s_add_u32 s28, s71, s52
	s_waitcnt lgkmcnt(0)
	v_mfma_f32_16x16x32_bf16 v[70:73], v[70:73], v[46:49], 0
	ds_read_b128 v[126:129], v79 offset:57536
	ds_read_b128 v[46:49], v79 offset:58048
	v_add_u32_e32 v79, 0x7800, v78
	ds_read2_b64 v[118:121], v79 offset0:192 offset1:196
	ds_read_b64 v[78:79], v78 offset:32320
	s_nop 2
	v_xor_b32_e32 v83, 0x80000000, v70
	s_waitcnt lgkmcnt(2)
	v_pk_mul_f32 v[108:109], v[128:129], v[48:49]
	v_pk_mul_f32 v[114:115], v[126:127], v[46:47]
	v_cndmask_b32_e64 v109, v129, v109, s[38:39]
	v_cndmask_b32_e64 v108, v128, v108, s[38:39]
	v_pk_mul_f32 v[116:117], v[108:109], v[84:85]
	v_xor_b32_e32 v84, 0x80000000, v71
	v_bfe_u32 v85, v84, 16, 1
	v_add3_u32 v84, v84, v85, s81
	v_cndmask_b32_e64 v115, v127, v115, s[38:39]
	v_cndmask_b32_e64 v114, v126, v114, s[38:39]
	v_cvt_pk_bf16_f32 v83, v83, v83
	v_pk_mul_f32 v[114:115], v[114:115], v[80:81]
	v_xor_b32_e32 v81, 0x80000000, v73
	v_lshrrev_b32_e32 v83, 16, v83
	s_waitcnt lgkmcnt(1)
	v_mfma_f32_16x16x32_bf16 v[74:77], v[118:121], v[74:77], v[114:117]
	v_xor_b32_e32 v80, 0x80000000, v72
	s_addc_u32 s29, s18, s53
	s_add_u32 s2, s19, s52
	v_and_or_b32 v114, v84, s80, v83
	v_cvt_pk_bf16_f32 v81, v81, v81
	v_cvt_pk_bf16_f32 v80, v80, v80
	v_lshrrev_b32_e32 v80, 16, v80
	v_and_or_b32 v115, v81, s80, v80
	v_mov_b32_e32 v80, v35
	v_mov_b32_e32 v81, v35
	v_mov_b32_e32 v116, v35
	v_mov_b32_e32 v117, v35
	v_lshlrev_b32_e32 v32, 2, v82
	s_addc_u32 s3, s66, s53
	s_waitcnt lgkmcnt(0)
	v_mfma_f32_16x16x32_bf16 v[74:77], v[78:81], v[114:117], v[74:77]
	ds_read_b64 v[78:79], v33 offset:55296
	s_add_u32 s52, s21, s52
	s_addc_u32 s53, s70, s53
	s_and_b64 vcc, exec, s[48:49]
	s_nop 3
	v_cvt_pk_bf16_f32 v74, v74, v75
	v_cvt_pk_bf16_f32 v75, v76, v77
	v_cvt_pk_bf16_f32 v62, v62, v63
	v_cvt_pk_bf16_f32 v63, v64, v65
	v_cvt_pk_bf16_f32 v64, v66, v67
	v_cvt_pk_bf16_f32 v65, v68, v69
	v_mov_b32_e32 v76, v35
	v_mov_b32_e32 v77, v35
	s_waitcnt lgkmcnt(0)
	s_nop 0
	v_mfma_f32_16x16x32_bf16 v[74:77], v[78:81], v[74:77], 0
	v_cvt_pk_bf16_f32 v66, v70, v71
	v_cvt_pk_bf16_f32 v67, v72, v73
	s_nop 5
	v_cvt_pk_bf16_f32 v68, v74, v75
	v_cvt_pk_bf16_f32 v69, v76, v77
	v_ashrrev_i32_e32 v33, 31, v32
	v_lshlrev_b32_e32 v70, 7, v45
	v_mov_b32_e32 v71, v35
	v_lshlrev_b64 v[74:75], 1, v[32:33]
	v_mul_u32_u24_e32 v33, 0x48, v106
	v_lshl_add_u64 v[72:73], s[28:29], 0, v[70:71]
	v_lshl_add_u64 v[70:71], s[52:53], 0, v[70:71]
	v_lshl_add_u32 v33, v33, 1, v86
	v_lshl_add_u64 v[80:81], v[72:73], 0, v[74:75]
	v_lshl_add_u64 v[78:79], v[70:71], 0, v[74:75]
	v_add_u32_e32 v74, 0x9000, v33
	ds_read2_b64 v[70:73], v74 offset1:4
	ds_read2_b64 v[74:77], v74 offset0:8 offset1:12
	s_waitcnt lgkmcnt(1)
	v_mfma_f32_16x16x32_bf16 v[70:73], v[70:73], v[62:65], 0
	v_add_u32_e32 v33, 0xb000, v33
	ds_read2_b64 v[106:109], v33 offset0:136 offset1:140
	s_mov_b64 s[28:29], -1
	s_waitcnt lgkmcnt(1)
	v_mfma_f32_16x16x32_bf16 v[70:73], v[74:77], v[66:69], v[70:73]
	ds_read2_b64 v[74:77], v33 offset0:128 offset1:132
	s_waitcnt lgkmcnt(0)
	v_mfma_f32_16x16x32_bf16 v[74:77], v[74:77], v[62:65], 0
	v_mfma_f32_16x16x32_bf16 v[74:77], v[106:109], v[66:69], v[74:77]
	s_cbranch_vccnz .LBB0_1783
	s_nop 2
	v_cvt_pk_bf16_f32 v84, v70, v71
	v_cvt_pk_bf16_f32 v85, v72, v73
	global_store_dwordx2 v[80:81], v[84:85], off
	s_nop 0
	v_cvt_pk_bf16_f32 v84, v74, v75
	v_cvt_pk_bf16_f32 v85, v76, v77
	s_mov_b64 s[28:29], 0
	global_store_dwordx2 v[78:79], v[84:85], off
